# K1: both 256B halves of each codebook row segment now requested together (tile-pair load issue, q-interleaved), waits regenerated
# baseline (speedup 1.0000x reference)
.LBB0_6:
	s_or_saveexec_b64 s[14:15], s[4:5]
	v_and_b32_e32 v194, 63, v0
	s_bfe_u32 s17, s2, 0x30003
	v_mov_b32_e32 v195, 0
	v_mov_b32_e32 v58, 0
	v_mov_b32_e32 v59, 0
	v_mov_b32_e32 v60, 0
	v_mov_b32_e32 v61, 0
	v_mov_b32_e32 v62, 0
	v_mov_b32_e32 v63, 0
	v_mov_b32_e32 v64, 0
	v_mov_b32_e32 v65, 0
	v_mov_b32_e32 v74, 0
	v_mov_b32_e32 v75, 0
	v_mov_b32_e32 v76, 0
	v_mov_b32_e32 v77, 0
	v_mov_b32_e32 v78, 0
	v_mov_b32_e32 v79, 0
	v_mov_b32_e32 v80, 0
	v_mov_b32_e32 v81, 0
	v_mov_b32_e32 v82, 0
	v_mov_b32_e32 v83, 0
	v_mov_b32_e32 v84, 0
	v_mov_b32_e32 v85, 0
	v_mov_b32_e32 v86, 0
	v_mov_b32_e32 v87, 0
	v_mov_b32_e32 v88, 0
	v_mov_b32_e32 v89, 0
	v_mov_b32_e32 v90, 0
	v_mov_b32_e32 v91, 0
	v_mov_b32_e32 v92, 0
	v_mov_b32_e32 v93, 0
	v_mov_b32_e32 v94, 0
	v_mov_b32_e32 v95, 0
	v_mov_b32_e32 v96, 0
	v_mov_b32_e32 v97, 0
	v_mov_b32_e32 v98, 0
	v_mov_b32_e32 v99, 0
	v_mov_b32_e32 v100, 0
	v_mov_b32_e32 v101, 0
	v_mov_b32_e32 v102, 0
	v_mov_b32_e32 v103, 0
	v_mov_b32_e32 v104, 0
	v_mov_b32_e32 v105, 0
	v_mov_b32_e32 v106, 0
	v_mov_b32_e32 v107, 0
	v_mov_b32_e32 v108, 0
	v_mov_b32_e32 v109, 0
	v_mov_b32_e32 v110, 0
	v_mov_b32_e32 v111, 0
	v_mov_b32_e32 v112, 0
	v_mov_b32_e32 v113, 0
	v_mov_b32_e32 v114, 0
	v_mov_b32_e32 v115, 0
	v_mov_b32_e32 v116, 0
	v_mov_b32_e32 v117, 0
	v_mov_b32_e32 v118, 0
	v_mov_b32_e32 v119, 0
	v_mov_b32_e32 v120, 0
	v_mov_b32_e32 v121, 0
	v_mov_b32_e32 v2, 0
	v_mov_b32_e32 v3, 0
	v_mov_b32_e32 v4, 0
	v_mov_b32_e32 v5, 0
	v_mov_b32_e32 v6, 0
	v_mov_b32_e32 v7, 0
	v_mov_b32_e32 v8, 0
	v_mov_b32_e32 v9, 0
	s_xor_b64 exec, exec, s[14:15]
	s_cbranch_execz .LBB0_8
	v_add_lshl_u32 v36, s3, v1, 7
	v_mul_u32_u24_e32 v82, 0x1f400, v130
	v_mov_b32_e32 v83, 0
	v_ashrrev_i32_e32 v37, 31, v36
	s_waitcnt lgkmcnt(0)
	v_lshl_add_u64 v[2:3], s[20:21], 0, v[82:83]
	v_lshl_add_u64 v[2:3], v[36:37], 2, v[2:3]
	v_and_b32_e32 v82, 48, v194
	v_lshl_add_u64 v[2:3], v[2:3], 0, v[82:83]
	s_mov_b32 s2, 0x1f4000
	v_add_co_u32_e32 v240, vcc, s2, v2
	v_lshrrev_b32_e32 v83, 4, v194
	s_nop 0
	v_addc_co_u32_e32 v241, vcc, 0, v3, vcc
	global_load_dwordx4 v[166:169], v[2:3], off
	global_load_dwordx4 v[170:173], v[2:3], off offset:64
	global_load_dwordx4 v[174:177], v[2:3], off offset:128
	global_load_dwordx4 v[178:181], v[2:3], off offset:192
	global_load_dwordx4 v[182:185], v[2:3], off offset:256
	global_load_dwordx4 v[186:189], v[2:3], off offset:320
	global_load_dwordx4 v[190:193], v[2:3], off offset:384
	global_load_dwordx4 v[204:207], v[2:3], off offset:448
	global_load_dwordx4 v[208:211], v[240:241], off
	global_load_dwordx4 v[212:215], v[240:241], off offset:64
	global_load_dwordx4 v[216:219], v[240:241], off offset:128
	global_load_dwordx4 v[220:223], v[240:241], off offset:192
	global_load_dwordx4 v[224:227], v[240:241], off offset:256
	global_load_dwordx4 v[228:231], v[240:241], off offset:320
	global_load_dwordx4 v[232:235], v[240:241], off offset:384
	global_load_dwordx4 v[236:239], v[240:241], off offset:448
	v_lshl_or_b32 v37, s17, 7, v83
	s_movk_i32 s3, 0x7d00
	v_mad_u32_u24 v36, v37, s3, v36
	v_lshlrev_b32_e32 v96, 4, v130
	s_and_b32 s9, s23, 0xffff
	s_mov_b32 s11, 0x20000
	s_mov_b32 s10, 0x7d00000
	s_mov_b32 s8, s22
	v_lshl_or_b32 v201, v36, 2, v96
	buffer_load_dwordx4 v[158:161], v201, s[8:11], 0 offen nt
	s_mov_b32 s18, 0x100
	buffer_load_dwordx4 v[136:139], v201, s[8:11], s18 offen nt
	s_mov_b32 s18, 0x7d000
	buffer_load_dwordx4 v[122:125], v201, s[8:11], s18 offen nt
	s_mov_b32 s18, 0x7d100
	buffer_load_dwordx4 v[140:143], v201, s[8:11], s18 offen nt
	s_mov_b32 s18, 0xfa000
	buffer_load_dwordx4 v[126:129], v201, s[8:11], s18 offen nt
	s_mov_b32 s18, 0xfa100
	buffer_load_dwordx4 v[154:157], v201, s[8:11], s18 offen nt
	s_mov_b32 s18, 0x177000
	buffer_load_dwordx4 v[132:135], v201, s[8:11], s18 offen nt
	s_mov_b32 s18, 0x177100
	buffer_load_dwordx4 v[162:165], v201, s[8:11], s18 offen nt
	s_mov_b32 s18, 0x1f4000
	buffer_load_dwordx4 v[58:61], v201, s[8:11], s18 offen nt
	s_mov_b32 s18, 0x1f4100
	buffer_load_dwordx4 v[106:109], v201, s[8:11], s18 offen nt
	s_mov_b32 s18, 0x271000
	buffer_load_dwordx4 v[62:65], v201, s[8:11], s18 offen nt
	s_mov_b32 s18, 0x271100
	buffer_load_dwordx4 v[110:113], v201, s[8:11], s18 offen nt
	s_mov_b32 s18, 0x2ee000
	buffer_load_dwordx4 v[98:101], v201, s[8:11], s18 offen nt
	s_mov_b32 s18, 0x2ee100
	buffer_load_dwordx4 v[146:149], v201, s[8:11], s18 offen nt
	s_mov_b32 s18, 0x36b000
	buffer_load_dwordx4 v[102:105], v201, s[8:11], s18 offen nt
	s_mov_b32 s18, 0x36b100
	buffer_load_dwordx4 v[150:153], v201, s[8:11], s18 offen nt
	v_mul_u32_u24_e32 v86, 0x120, v130
	v_mul_u32_u24_e32 v84, 0x2400, v1
	v_mul_u32_u24_e32 v85, 0x120, v83
	v_add3_u32 v200, v84, v85, v96
	s_waitcnt vmcnt(30)
	v_cvt_pk_bf16_f32 v22, v166, v167
	v_cvt_pk_bf16_f32 v23, v168, v169
	v_cvt_pk_bf16_f32 v24, v170, v171
	v_cvt_pk_bf16_f32 v25, v172, v173
	v_lshlrev_b32_e32 v242, 16, v22
	v_and_b32_e32 v243, 0xffff0000, v22
	v_lshlrev_b32_e32 v244, 16, v23
	v_and_b32_e32 v245, 0xffff0000, v23
	v_lshlrev_b32_e32 v246, 16, v24
	v_and_b32_e32 v247, 0xffff0000, v24
	v_lshlrev_b32_e32 v248, 16, v25
	v_and_b32_e32 v249, 0xffff0000, v25
	v_pk_add_f32 v[242:243], v[166:167], v[242:243] neg_lo:[0,1] neg_hi:[0,1]
	v_pk_add_f32 v[244:245], v[168:169], v[244:245] neg_lo:[0,1] neg_hi:[0,1]
	v_pk_add_f32 v[246:247], v[170:171], v[246:247] neg_lo:[0,1] neg_hi:[0,1]
	v_pk_add_f32 v[248:249], v[172:173], v[248:249] neg_lo:[0,1] neg_hi:[0,1]
	v_cvt_pk_bf16_f32 v30, v242, v243
	v_cvt_pk_bf16_f32 v31, v244, v245
	v_cvt_pk_bf16_f32 v32, v246, v247
	v_cvt_pk_bf16_f32 v33, v248, v249
	s_waitcnt vmcnt(28)
	v_cvt_pk_bf16_f32 v18, v174, v175
	v_cvt_pk_bf16_f32 v19, v176, v177
	v_cvt_pk_bf16_f32 v20, v178, v179
	v_cvt_pk_bf16_f32 v21, v180, v181
	v_lshlrev_b32_e32 v242, 16, v18
	v_and_b32_e32 v243, 0xffff0000, v18
	v_lshlrev_b32_e32 v244, 16, v19
	v_and_b32_e32 v245, 0xffff0000, v19
	v_lshlrev_b32_e32 v246, 16, v20
	v_and_b32_e32 v247, 0xffff0000, v20
	v_lshlrev_b32_e32 v248, 16, v21
	v_and_b32_e32 v249, 0xffff0000, v21
	v_pk_add_f32 v[242:243], v[174:175], v[242:243] neg_lo:[0,1] neg_hi:[0,1]
	v_pk_add_f32 v[244:245], v[176:177], v[244:245] neg_lo:[0,1] neg_hi:[0,1]
	v_pk_add_f32 v[246:247], v[178:179], v[246:247] neg_lo:[0,1] neg_hi:[0,1]
	v_pk_add_f32 v[248:249], v[180:181], v[248:249] neg_lo:[0,1] neg_hi:[0,1]
	v_cvt_pk_bf16_f32 v26, v242, v243
	v_cvt_pk_bf16_f32 v27, v244, v245
	v_cvt_pk_bf16_f32 v28, v246, v247
	v_cvt_pk_bf16_f32 v29, v248, v249
	s_waitcnt vmcnt(26)
	v_cvt_pk_bf16_f32 v6, v182, v183
	v_cvt_pk_bf16_f32 v7, v184, v185
	v_cvt_pk_bf16_f32 v8, v186, v187
	v_cvt_pk_bf16_f32 v9, v188, v189
	v_lshlrev_b32_e32 v242, 16, v6
	v_and_b32_e32 v243, 0xffff0000, v6
	v_lshlrev_b32_e32 v244, 16, v7
	v_and_b32_e32 v245, 0xffff0000, v7
	v_lshlrev_b32_e32 v246, 16, v8
	v_and_b32_e32 v247, 0xffff0000, v8
	v_lshlrev_b32_e32 v248, 16, v9
	v_and_b32_e32 v249, 0xffff0000, v9
	v_pk_add_f32 v[242:243], v[182:183], v[242:243] neg_lo:[0,1] neg_hi:[0,1]
	v_pk_add_f32 v[244:245], v[184:185], v[244:245] neg_lo:[0,1] neg_hi:[0,1]
	v_pk_add_f32 v[246:247], v[186:187], v[246:247] neg_lo:[0,1] neg_hi:[0,1]
	v_pk_add_f32 v[248:249], v[188:189], v[248:249] neg_lo:[0,1] neg_hi:[0,1]
	v_cvt_pk_bf16_f32 v14, v242, v243
	v_cvt_pk_bf16_f32 v15, v244, v245
	v_cvt_pk_bf16_f32 v16, v246, v247
	v_cvt_pk_bf16_f32 v17, v248, v249
	s_waitcnt vmcnt(24)
	v_cvt_pk_bf16_f32 v2, v190, v191
	v_cvt_pk_bf16_f32 v3, v192, v193
	v_cvt_pk_bf16_f32 v4, v204, v205
	v_cvt_pk_bf16_f32 v5, v206, v207
	v_lshlrev_b32_e32 v242, 16, v2
	v_and_b32_e32 v243, 0xffff0000, v2
	v_lshlrev_b32_e32 v244, 16, v3
	v_and_b32_e32 v245, 0xffff0000, v3
	v_lshlrev_b32_e32 v246, 16, v4
	v_and_b32_e32 v247, 0xffff0000, v4
	v_lshlrev_b32_e32 v248, 16, v5
	v_and_b32_e32 v249, 0xffff0000, v5
	v_pk_add_f32 v[242:243], v[190:191], v[242:243] neg_lo:[0,1] neg_hi:[0,1]
	v_pk_add_f32 v[244:245], v[192:193], v[244:245] neg_lo:[0,1] neg_hi:[0,1]
	v_pk_add_f32 v[246:247], v[204:205], v[246:247] neg_lo:[0,1] neg_hi:[0,1]
	v_pk_add_f32 v[248:249], v[206:207], v[248:249] neg_lo:[0,1] neg_hi:[0,1]
	v_cvt_pk_bf16_f32 v10, v242, v243
	v_cvt_pk_bf16_f32 v11, v244, v245
	v_cvt_pk_bf16_f32 v12, v246, v247
	v_cvt_pk_bf16_f32 v13, v248, v249
	s_waitcnt vmcnt(22)
	v_cvt_pk_bf16_f32 v34, v208, v209
	v_cvt_pk_bf16_f32 v35, v210, v211
	v_cvt_pk_bf16_f32 v36, v212, v213
	v_cvt_pk_bf16_f32 v37, v214, v215
	v_lshlrev_b32_e32 v242, 16, v34
	v_and_b32_e32 v243, 0xffff0000, v34
	v_lshlrev_b32_e32 v244, 16, v35
	v_and_b32_e32 v245, 0xffff0000, v35
	v_lshlrev_b32_e32 v246, 16, v36
	v_and_b32_e32 v247, 0xffff0000, v36
	v_lshlrev_b32_e32 v248, 16, v37
	v_and_b32_e32 v249, 0xffff0000, v37
	v_pk_add_f32 v[242:243], v[208:209], v[242:243] neg_lo:[0,1] neg_hi:[0,1]
	v_pk_add_f32 v[244:245], v[210:211], v[244:245] neg_lo:[0,1] neg_hi:[0,1]
	v_pk_add_f32 v[246:247], v[212:213], v[246:247] neg_lo:[0,1] neg_hi:[0,1]
	v_pk_add_f32 v[248:249], v[214:215], v[248:249] neg_lo:[0,1] neg_hi:[0,1]
	v_cvt_pk_bf16_f32 v38, v242, v243
	v_cvt_pk_bf16_f32 v39, v244, v245
	v_cvt_pk_bf16_f32 v40, v246, v247
	v_cvt_pk_bf16_f32 v41, v248, v249
	s_waitcnt vmcnt(20)
	v_cvt_pk_bf16_f32 v66, v216, v217
	v_cvt_pk_bf16_f32 v67, v218, v219
	v_cvt_pk_bf16_f32 v68, v220, v221
	v_cvt_pk_bf16_f32 v69, v222, v223
	v_lshlrev_b32_e32 v242, 16, v66
	v_and_b32_e32 v243, 0xffff0000, v66
	v_lshlrev_b32_e32 v244, 16, v67
	v_and_b32_e32 v245, 0xffff0000, v67
	v_lshlrev_b32_e32 v246, 16, v68
	v_and_b32_e32 v247, 0xffff0000, v68
	v_lshlrev_b32_e32 v248, 16, v69
	v_and_b32_e32 v249, 0xffff0000, v69
	v_pk_add_f32 v[242:243], v[216:217], v[242:243] neg_lo:[0,1] neg_hi:[0,1]
	v_pk_add_f32 v[244:245], v[218:219], v[244:245] neg_lo:[0,1] neg_hi:[0,1]
	v_pk_add_f32 v[246:247], v[220:221], v[246:247] neg_lo:[0,1] neg_hi:[0,1]
	v_pk_add_f32 v[248:249], v[222:223], v[248:249] neg_lo:[0,1] neg_hi:[0,1]
	v_cvt_pk_bf16_f32 v70, v242, v243
	v_cvt_pk_bf16_f32 v71, v244, v245
	v_cvt_pk_bf16_f32 v72, v246, v247
	v_cvt_pk_bf16_f32 v73, v248, v249
	s_waitcnt vmcnt(18)
	v_cvt_pk_bf16_f32 v50, v224, v225
	v_cvt_pk_bf16_f32 v51, v226, v227
	v_cvt_pk_bf16_f32 v52, v228, v229
	v_cvt_pk_bf16_f32 v53, v230, v231
	v_lshlrev_b32_e32 v242, 16, v50
	v_and_b32_e32 v243, 0xffff0000, v50
	v_lshlrev_b32_e32 v244, 16, v51
	v_and_b32_e32 v245, 0xffff0000, v51
	v_lshlrev_b32_e32 v246, 16, v52
	v_and_b32_e32 v247, 0xffff0000, v52
	v_lshlrev_b32_e32 v248, 16, v53
	v_and_b32_e32 v249, 0xffff0000, v53
	v_pk_add_f32 v[242:243], v[224:225], v[242:243] neg_lo:[0,1] neg_hi:[0,1]
	v_pk_add_f32 v[244:245], v[226:227], v[244:245] neg_lo:[0,1] neg_hi:[0,1]
	v_pk_add_f32 v[246:247], v[228:229], v[246:247] neg_lo:[0,1] neg_hi:[0,1]
	v_pk_add_f32 v[248:249], v[230:231], v[248:249] neg_lo:[0,1] neg_hi:[0,1]
	v_cvt_pk_bf16_f32 v54, v242, v243
	v_cvt_pk_bf16_f32 v55, v244, v245
	v_cvt_pk_bf16_f32 v56, v246, v247
	v_cvt_pk_bf16_f32 v57, v248, v249
	s_waitcnt vmcnt(16)
	v_cvt_pk_bf16_f32 v42, v232, v233
	v_cvt_pk_bf16_f32 v43, v234, v235
	v_cvt_pk_bf16_f32 v44, v236, v237
	v_cvt_pk_bf16_f32 v45, v238, v239
	v_lshlrev_b32_e32 v242, 16, v42
	v_and_b32_e32 v243, 0xffff0000, v42
	v_lshlrev_b32_e32 v244, 16, v43
	v_and_b32_e32 v245, 0xffff0000, v43
	v_lshlrev_b32_e32 v246, 16, v44
	v_and_b32_e32 v247, 0xffff0000, v44
	v_lshlrev_b32_e32 v248, 16, v45
	v_and_b32_e32 v249, 0xffff0000, v45
	v_pk_add_f32 v[242:243], v[232:233], v[242:243] neg_lo:[0,1] neg_hi:[0,1]
	v_pk_add_f32 v[244:245], v[234:235], v[244:245] neg_lo:[0,1] neg_hi:[0,1]
	v_pk_add_f32 v[246:247], v[236:237], v[246:247] neg_lo:[0,1] neg_hi:[0,1]
	v_pk_add_f32 v[248:249], v[238:239], v[248:249] neg_lo:[0,1] neg_hi:[0,1]
	v_cvt_pk_bf16_f32 v46, v242, v243
	v_cvt_pk_bf16_f32 v47, v244, v245
	v_cvt_pk_bf16_f32 v48, v246, v247
	v_cvt_pk_bf16_f32 v49, v248, v249
	s_waitcnt vmcnt(15)
	ds_write_b128 v200, v[158:161]
	s_waitcnt vmcnt(13)
	ds_write_b128 v200, v[122:125] offset:1152
	s_waitcnt vmcnt(11)
	ds_write_b128 v200, v[126:129] offset:2304
	s_waitcnt vmcnt(9)
	ds_write_b128 v200, v[132:135] offset:3456
	v_add3_u32 v197, v84, v86, v82
	ds_read_b128 v[90:93], v197
	ds_read_b128 v[94:97], v197 offset:64
	ds_read_b128 v[132:135], v197 offset:128
	ds_read_b128 v[158:161], v197 offset:192
	v_lshrrev_b32_e32 v82, 2, v130
	v_and_b32_e32 v84, 3, v0
	v_cmp_eq_u32_e32 vcc, v83, v82
	v_or_b32_e32 v196, 0x800, v0
	s_nop 0
	v_cndmask_b32_e32 v82, 4, v84, vcc
	v_cmp_eq_u32_e64 s[6:7], 0, v82
	v_cmp_eq_u32_e64 s[4:5], 1, v82
	v_cmp_eq_u32_e64 s[2:3], 2, v82
	v_cmp_eq_u32_e32 vcc, 3, v82
	s_mov_b32 s18, 0x3e8000
	buffer_load_dwordx4 v[74:77], v201, s[8:11], s18 offen nt
	s_mov_b32 s18, 0x3e8100
	buffer_load_dwordx4 v[82:85], v201, s[8:11], s18 offen nt
	s_mov_b32 s18, 0x465000
	buffer_load_dwordx4 v[78:81], v201, s[8:11], s18 offen nt
	s_mov_b32 s18, 0x465100
	buffer_load_dwordx4 v[86:89], v201, s[8:11], s18 offen nt
	s_mov_b32 s18, 0x4e2000
	buffer_load_dwordx4 v[114:117], v201, s[8:11], s18 offen nt
	s_mov_b32 s18, 0x4e2100
	buffer_load_dwordx4 v[122:125], v201, s[8:11], s18 offen nt
	s_mov_b32 s18, 0x55f000
	buffer_load_dwordx4 v[118:121], v201, s[8:11], s18 offen nt
	s_mov_b32 s18, 0x55f100
	buffer_load_dwordx4 v[126:129], v201, s[8:11], s18 offen nt
	s_waitcnt vmcnt(22)
	ds_write_b128 v200, v[136:139] offset:4608
	s_waitcnt vmcnt(20)
	ds_write_b128 v200, v[140:143] offset:5760
	s_waitcnt vmcnt(18)
	ds_write_b128 v200, v[154:157] offset:6912
	s_waitcnt vmcnt(16)
	ds_write_b128 v200, v[162:165] offset:8064
	s_waitcnt lgkmcnt(7)
	v_cvt_pk_bf16_f32 v136, v90, v91
	v_cvt_pk_bf16_f32 v137, v92, v93
	s_waitcnt lgkmcnt(6)
	v_cvt_pk_bf16_f32 v138, v94, v95
	v_cvt_pk_bf16_f32 v139, v96, v97
	v_lshlrev_b32_e32 v144, 16, v136
	v_and_b32_e32 v145, 0xffff0000, v136
	v_mfma_f32_16x16x32_bf16 v[140:143], v[22:25], v[136:139], 0
	v_add_f32_e64 v90, v90, -v144
	v_add_f32_e64 v91, v91, -v145
	v_lshlrev_b32_e32 v144, 16, v137
	v_and_b32_e32 v145, 0xffff0000, v137
	v_mfma_f32_16x16x32_bf16 v[154:157], v[34:37], v[136:139], 0
	v_add_f32_e64 v92, v92, -v144
	v_add_f32_e64 v93, v93, -v145
	v_cvt_pk_bf16_f32 v90, v90, v91
	v_cvt_pk_bf16_f32 v91, v92, v93
	v_lshlrev_b32_e32 v92, 16, v138
	v_and_b32_e32 v93, 0xffff0000, v138
	v_mfma_f32_16x16x32_bf16 v[140:143], v[30:33], v[136:139], v[140:143]
	v_add_f32_e64 v92, v94, -v92
	v_add_f32_e64 v93, v95, -v93
	v_lshlrev_b32_e32 v94, 16, v139
	v_and_b32_e32 v95, 0xffff0000, v139
	v_mfma_f32_16x16x32_bf16 v[154:157], v[38:41], v[136:139], v[154:157]
	v_add_f32_e64 v94, v96, -v94
	v_add_f32_e64 v95, v97, -v95
	v_cvt_pk_bf16_f32 v92, v92, v93
	v_cvt_pk_bf16_f32 v93, v94, v95
	v_mfma_f32_16x16x32_bf16 v[162:165], v[136:139], v[136:139], 0
	v_lshl_or_b32 v199, v1, 8, v130
	v_cndmask_b32_e64 v130, v196, v199, s[6:7]
	v_mov_b32_e32 v198, 0x20000
	v_mfma_f32_16x16x32_bf16 v[94:97], v[136:139], v[90:93], 0
	v_lshl_or_b32 v130, v130, 2, v198
	v_mfma_f32_16x16x32_bf16 v[136:139], v[22:25], v[90:93], v[140:143]
	v_mfma_f32_16x16x32_bf16 v[90:93], v[34:37], v[90:93], v[154:157]
	s_waitcnt lgkmcnt(5)
	s_nop 0
	v_cvt_pk_bf16_f32 v140, v132, v133
	v_lshlrev_b32_e32 v142, 16, v140
	v_and_b32_e32 v143, 0xffff0000, v140
	v_pk_add_f32 v[132:133], v[132:133], v[142:143] neg_lo:[0,1] neg_hi:[0,1]
	v_cvt_pk_bf16_f32 v141, v134, v135
	s_waitcnt lgkmcnt(4)
	v_cvt_pk_bf16_f32 v142, v158, v159
	v_cvt_pk_bf16_f32 v143, v160, v161
	v_lshlrev_b32_e32 v144, 16, v141
	v_and_b32_e32 v145, 0xffff0000, v141
	v_mfma_f32_16x16x32_bf16 v[90:93], v[66:69], v[140:143], v[90:93]
	v_add_f32_e64 v134, v134, -v144
	v_add_f32_e64 v135, v135, -v145
	v_cvt_pk_bf16_f32 v132, v132, v133
	v_cvt_pk_bf16_f32 v133, v134, v135
	v_lshlrev_b32_e32 v134, 16, v142
	v_and_b32_e32 v135, 0xffff0000, v142
	v_lshlrev_b32_e32 v144, 16, v143
	v_and_b32_e32 v145, 0xffff0000, v143
	v_pk_add_f32 v[134:135], v[158:159], v[134:135] neg_lo:[0,1] neg_hi:[0,1]
	v_pk_add_f32 v[144:145], v[160:161], v[144:145] neg_lo:[0,1] neg_hi:[0,1]
	v_mfma_f32_16x16x32_bf16 v[136:139], v[18:21], v[140:143], v[136:139]
	v_cvt_pk_bf16_f32 v134, v134, v135
	v_cvt_pk_bf16_f32 v135, v144, v145
	v_mfma_f32_16x16x32_bf16 v[90:93], v[70:73], v[140:143], v[90:93]
	v_mfma_f32_16x16x32_bf16 v[154:157], v[140:143], v[140:143], v[162:165]
	v_mfma_f32_16x16x32_bf16 v[94:97], v[140:143], v[132:135], v[94:97]
	v_mfma_f32_16x16x32_bf16 v[136:139], v[26:29], v[140:143], v[136:139]
	v_mfma_f32_16x16x32_bf16 v[142:145], v[66:69], v[132:135], v[90:93]
	s_nop 5
	v_fma_f32 v94, v94, 2.0, v154
	v_fma_f32 v95, v95, 2.0, v155
	ds_write_b32 v130, v94
	v_pk_fma_f32 v[96:97], v[96:97], 2.0, v[156:157] op_sel_hi:[1,0,1]
	v_cndmask_b32_e64 v90, v196, v199, s[4:5]
	v_lshl_or_b32 v90, v90, 2, v198
	ds_write_b32 v90, v95
	v_cndmask_b32_e64 v90, v196, v199, s[2:3]
	v_lshl_or_b32 v90, v90, 2, v198
	ds_write_b32 v90, v96
	v_cndmask_b32_e32 v90, v196, v199, vcc
	v_lshl_or_b32 v90, v90, 2, v198
	v_mfma_f32_16x16x32_bf16 v[138:141], v[18:21], v[132:135], v[136:139]
	ds_write_b32 v90, v97
	ds_read_b128 v[154:157], v197 offset:4608
	ds_read_b128 v[158:161], v197 offset:4672
	ds_read_b128 v[162:165], v197 offset:4736
	ds_read_b128 v[166:169], v197 offset:4800
	s_waitcnt vmcnt(15)
	ds_write_b128 v200, v[58:61]
	s_waitcnt vmcnt(13)
	ds_write_b128 v200, v[62:65] offset:1152
	s_waitcnt vmcnt(11)
	ds_write_b128 v200, v[98:101] offset:2304
	s_waitcnt vmcnt(9)
	ds_write_b128 v200, v[102:105] offset:3456
	s_waitcnt lgkmcnt(7)
	v_cvt_pk_bf16_f32 v58, v154, v155
	v_cvt_pk_bf16_f32 v59, v156, v157
	s_waitcnt lgkmcnt(6)
	v_cvt_pk_bf16_f32 v60, v158, v159
	v_cvt_pk_bf16_f32 v61, v160, v161
	v_lshlrev_b32_e32 v98, 16, v58
	v_and_b32_e32 v99, 0xffff0000, v58
	v_mfma_f32_16x16x32_bf16 v[62:65], v[6:9], v[58:61], v[138:141]
	v_lshlrev_b32_e32 v100, 16, v59
	v_and_b32_e32 v101, 0xffff0000, v59
	v_pk_add_f32 v[98:99], v[154:155], v[98:99] neg_lo:[0,1] neg_hi:[0,1]
	v_mfma_f32_16x16x32_bf16 v[102:105], v[50:53], v[58:61], v[142:145]
	v_add_f32_e64 v100, v156, -v100
	v_add_f32_e64 v101, v157, -v101
	v_cvt_pk_bf16_f32 v98, v98, v99
	v_cvt_pk_bf16_f32 v99, v100, v101
	v_mfma_f32_16x16x32_bf16 v[62:65], v[14:17], v[58:61], v[62:65]
	v_lshlrev_b32_e32 v100, 16, v60
	v_and_b32_e32 v101, 0xffff0000, v60
	v_lshlrev_b32_e32 v142, 16, v61
	v_and_b32_e32 v143, 0xffff0000, v61
	v_pk_add_f32 v[100:101], v[158:159], v[100:101] neg_lo:[0,1] neg_hi:[0,1]
	v_mfma_f32_16x16x32_bf16 v[102:105], v[54:57], v[58:61], v[102:105]
	v_add_f32_e64 v142, v160, -v142
	v_add_f32_e64 v143, v161, -v143
	v_cvt_pk_bf16_f32 v100, v100, v101
	v_cvt_pk_bf16_f32 v101, v142, v143
	s_waitcnt lgkmcnt(5)
	v_cvt_pk_bf16_f32 v142, v162, v163
	v_mfma_f32_16x16x32_bf16 v[138:141], v[58:61], v[58:61], 0
	v_lshlrev_b32_e32 v144, 16, v142
	v_and_b32_e32 v145, 0xffff0000, v142
	v_cvt_pk_bf16_f32 v143, v164, v165
	v_mfma_f32_16x16x32_bf16 v[62:65], v[6:9], v[98:101], v[62:65]
	v_mfma_f32_16x16x32_bf16 v[58:61], v[58:61], v[98:101], 0
	v_mfma_f32_16x16x32_bf16 v[98:101], v[50:53], v[98:101], v[102:105]
	s_nop 2
	v_add_f32_e64 v102, v162, -v144
	v_add_f32_e64 v103, v163, -v145
	s_waitcnt lgkmcnt(4)
	v_cvt_pk_bf16_f32 v144, v166, v167
	v_cvt_pk_bf16_f32 v145, v168, v169
	v_lshlrev_b32_e32 v104, 16, v143
	v_and_b32_e32 v105, 0xffff0000, v143
	v_mfma_f32_16x16x32_bf16 v[62:65], v[2:5], v[142:145], v[62:65]
	v_add_f32_e64 v104, v164, -v104
	v_add_f32_e64 v105, v165, -v105
	v_cvt_pk_bf16_f32 v102, v102, v103
	v_cvt_pk_bf16_f32 v103, v104, v105
	v_lshlrev_b32_e32 v104, 16, v144
	v_and_b32_e32 v105, 0xffff0000, v144
	v_lshlrev_b32_e32 v154, 16, v145
	v_and_b32_e32 v155, 0xffff0000, v145
	v_mfma_f32_16x16x32_bf16 v[98:101], v[42:45], v[142:145], v[98:101]
	v_add_f32_e64 v104, v166, -v104
	v_add_f32_e64 v105, v167, -v105
	v_pk_add_f32 v[154:155], v[168:169], v[154:155] neg_lo:[0,1] neg_hi:[0,1]
	v_cvt_pk_bf16_f32 v104, v104, v105
	v_cvt_pk_bf16_f32 v105, v154, v155
	v_mfma_f32_16x16x32_bf16 v[138:141], v[142:145], v[142:145], v[138:141]
	v_mfma_f32_16x16x32_bf16 v[62:65], v[10:13], v[142:145], v[62:65]
	v_mfma_f32_16x16x32_bf16 v[58:61], v[142:145], v[102:105], v[58:61]
	v_mfma_f32_16x16x32_bf16 v[98:101], v[46:49], v[142:145], v[98:101]
	v_or_b32_e32 v142, 0x80, v199
	v_cndmask_b32_e64 v143, v196, v142, s[6:7]
	s_nop 4
	v_pk_fma_f32 v[140:141], v[60:61], 2.0, v[140:141] op_sel_hi:[1,0,1]
	v_pk_fma_f32 v[138:139], v[58:59], 2.0, v[138:139] op_sel_hi:[1,0,1]
	v_mfma_f32_16x16x32_bf16 v[58:61], v[2:5], v[102:105], v[62:65]
	s_nop 2
	v_lshl_or_b32 v62, v143, 2, v198
	ds_write_b32 v62, v138
	v_cndmask_b32_e64 v138, v196, v142, s[4:5]
	v_mfma_f32_16x16x32_bf16 v[62:65], v[42:45], v[102:105], v[98:101]
	s_nop 2
	v_lshl_or_b32 v98, v138, 2, v198
	ds_write_b32 v98, v139
	v_cndmask_b32_e64 v98, v196, v142, s[2:3]
	v_lshl_or_b32 v98, v98, 2, v198
	ds_write_b32 v98, v140
	v_cndmask_b32_e32 v98, v196, v142, vcc
	v_lshl_or_b32 v98, v98, 2, v198
	ds_write_b32 v98, v141
	ds_read_b128 v[154:157], v197
	ds_read_b128 v[158:161], v197 offset:64
	ds_read_b128 v[162:165], v197 offset:128
	ds_read_b128 v[166:169], v197 offset:192
	s_mov_b32 s18, 0x5dc000
	buffer_load_dwordx4 v[90:93], v201, s[8:11], s18 offen nt
	s_mov_b32 s18, 0x5dc100
	buffer_load_dwordx4 v[98:101], v201, s[8:11], s18 offen nt
	s_mov_b32 s18, 0x659000
	buffer_load_dwordx4 v[94:97], v201, s[8:11], s18 offen nt
	s_mov_b32 s18, 0x659100
	buffer_load_dwordx4 v[102:105], v201, s[8:11], s18 offen nt
	s_mov_b32 s18, 0x6d6000
	buffer_load_dwordx4 v[130:133], v201, s[8:11], s18 offen nt
	s_mov_b32 s18, 0x6d6100
	buffer_load_dwordx4 v[138:141], v201, s[8:11], s18 offen nt
	s_mov_b32 s18, 0x753000
	buffer_load_dwordx4 v[134:137], v201, s[8:11], s18 offen nt
	s_mov_b32 s18, 0x753100
	buffer_load_dwordx4 v[142:145], v201, s[8:11], s18 offen nt
	s_waitcnt vmcnt(22)
	ds_write_b128 v200, v[106:109] offset:4608
	s_waitcnt vmcnt(20)
	ds_write_b128 v200, v[110:113] offset:5760
	s_waitcnt vmcnt(18)
	ds_write_b128 v200, v[146:149] offset:6912
	s_waitcnt vmcnt(16)
	ds_write_b128 v200, v[150:153] offset:8064
	s_waitcnt lgkmcnt(7)
	v_cvt_pk_bf16_f32 v106, v154, v155
	v_cvt_pk_bf16_f32 v107, v156, v157
	s_waitcnt lgkmcnt(6)
	v_cvt_pk_bf16_f32 v108, v158, v159
	v_cvt_pk_bf16_f32 v109, v160, v161
	v_lshlrev_b32_e32 v146, 16, v106
	v_and_b32_e32 v147, 0xffff0000, v106
	v_mfma_f32_16x16x32_bf16 v[110:113], v[22:25], v[106:109], 0
	v_lshlrev_b32_e32 v148, 16, v107
	v_and_b32_e32 v149, 0xffff0000, v107
	v_pk_add_f32 v[146:147], v[154:155], v[146:147] neg_lo:[0,1] neg_hi:[0,1]
	v_mfma_f32_16x16x32_bf16 v[150:153], v[34:37], v[106:109], 0
	v_add_f32_e64 v148, v156, -v148
	v_add_f32_e64 v149, v157, -v149
	v_cvt_pk_bf16_f32 v146, v146, v147
	v_cvt_pk_bf16_f32 v147, v148, v149
	v_lshlrev_b32_e32 v148, 16, v108
	v_and_b32_e32 v149, 0xffff0000, v108
	v_mfma_f32_16x16x32_bf16 v[110:113], v[30:33], v[106:109], v[110:113]
	v_add_f32_e64 v148, v158, -v148
	v_add_f32_e64 v149, v159, -v149
	v_lshlrev_b32_e32 v158, 16, v109
	v_and_b32_e32 v159, 0xffff0000, v109
	v_pk_add_f32 v[158:159], v[160:161], v[158:159] neg_lo:[0,1] neg_hi:[0,1]
	v_cvt_pk_bf16_f32 v148, v148, v149
	v_mfma_f32_16x16x32_bf16 v[150:153], v[38:41], v[106:109], v[150:153]
	v_cvt_pk_bf16_f32 v149, v158, v159
	s_waitcnt lgkmcnt(5)
	v_cvt_pk_bf16_f32 v158, v162, v163
	v_lshlrev_b32_e32 v160, 16, v158
	v_mfma_f32_16x16x32_bf16 v[110:113], v[22:25], v[146:149], v[110:113]
	v_and_b32_e32 v161, 0xffff0000, v158
	v_cvt_pk_bf16_f32 v159, v164, v165
	v_mfma_f32_16x16x32_bf16 v[154:157], v[106:109], v[106:109], 0
	v_mfma_f32_16x16x32_bf16 v[106:109], v[106:109], v[146:149], 0
	v_mfma_f32_16x16x32_bf16 v[146:149], v[34:37], v[146:149], v[150:153]
	s_nop 2
	v_add_f32_e64 v150, v162, -v160
	v_add_f32_e64 v151, v163, -v161
	s_waitcnt lgkmcnt(4)
	v_cvt_pk_bf16_f32 v160, v166, v167
	v_cvt_pk_bf16_f32 v161, v168, v169
	v_lshlrev_b32_e32 v152, 16, v159
	v_and_b32_e32 v153, 0xffff0000, v159
	v_mfma_f32_16x16x32_bf16 v[110:113], v[18:21], v[158:161], v[110:113]
	v_add_f32_e64 v152, v164, -v152
	v_add_f32_e64 v153, v165, -v153
	v_cvt_pk_bf16_f32 v150, v150, v151
	v_cvt_pk_bf16_f32 v151, v152, v153
	v_lshlrev_b32_e32 v152, 16, v160
	v_and_b32_e32 v153, 0xffff0000, v160
	v_lshlrev_b32_e32 v162, 16, v161
	v_and_b32_e32 v163, 0xffff0000, v161
	v_pk_add_f32 v[152:153], v[166:167], v[152:153] neg_lo:[0,1] neg_hi:[0,1]
	v_pk_add_f32 v[162:163], v[168:169], v[162:163] neg_lo:[0,1] neg_hi:[0,1]
	v_mfma_f32_16x16x32_bf16 v[146:149], v[66:69], v[158:161], v[146:149]
	v_cvt_pk_bf16_f32 v152, v152, v153
	v_cvt_pk_bf16_f32 v153, v162, v163
	v_or_b32_e32 v162, 16, v199
	v_mfma_f32_16x16x32_bf16 v[154:157], v[158:161], v[158:161], v[154:157]
	v_mfma_f32_16x16x32_bf16 v[110:113], v[26:29], v[158:161], v[110:113]
	v_mfma_f32_16x16x32_bf16 v[106:109], v[158:161], v[150:153], v[106:109]
	v_mfma_f32_16x16x32_bf16 v[146:149], v[70:73], v[158:161], v[146:149]
	v_cndmask_b32_e64 v158, v196, v162, s[6:7]
	s_nop 5
	v_pk_fma_f32 v[108:109], v[108:109], 2.0, v[156:157] op_sel_hi:[1,0,1]
	v_pk_fma_f32 v[106:107], v[106:107], 2.0, v[154:155] op_sel_hi:[1,0,1]
	v_mfma_f32_16x16x32_bf16 v[154:157], v[18:21], v[150:153], v[110:113]
	s_nop 2
	v_lshl_or_b32 v110, v158, 2, v198
	ds_write_b32 v110, v106
	v_cndmask_b32_e64 v106, v196, v162, s[4:5]
	v_lshl_or_b32 v106, v106, 2, v198
	ds_write_b32 v106, v107
	v_cndmask_b32_e64 v106, v196, v162, s[2:3]
	v_lshl_or_b32 v106, v106, 2, v198
	ds_write_b32 v106, v108
	v_cndmask_b32_e32 v106, v196, v162, vcc
	v_lshl_or_b32 v106, v106, 2, v198
	v_mfma_f32_16x16x32_bf16 v[158:161], v[66:69], v[150:153], v[146:149]
	ds_write_b32 v106, v109
	ds_read_b128 v[162:165], v197 offset:4608
	ds_read_b128 v[166:169], v197 offset:4672
	ds_read_b128 v[170:173], v197 offset:4736
	ds_read_b128 v[174:177], v197 offset:4800
	s_waitcnt vmcnt(15)
	ds_write_b128 v200, v[74:77]
	s_waitcnt vmcnt(13)
	ds_write_b128 v200, v[78:81] offset:1152
	s_waitcnt vmcnt(11)
	ds_write_b128 v200, v[114:117] offset:2304
	s_waitcnt vmcnt(9)
	ds_write_b128 v200, v[118:121] offset:3456
	s_waitcnt lgkmcnt(7)
	v_cvt_pk_bf16_f32 v74, v162, v163
	v_cvt_pk_bf16_f32 v75, v164, v165
	s_waitcnt lgkmcnt(6)
	v_cvt_pk_bf16_f32 v76, v166, v167
	v_cvt_pk_bf16_f32 v77, v168, v169
	v_lshlrev_b32_e32 v114, 16, v74
	v_and_b32_e32 v115, 0xffff0000, v74
	v_mfma_f32_16x16x32_bf16 v[78:81], v[6:9], v[74:77], v[154:157]
	v_lshlrev_b32_e32 v116, 16, v75
	v_and_b32_e32 v117, 0xffff0000, v75
	v_pk_add_f32 v[114:115], v[162:163], v[114:115] neg_lo:[0,1] neg_hi:[0,1]
	v_mfma_f32_16x16x32_bf16 v[118:121], v[50:53], v[74:77], v[158:161]
	v_add_f32_e64 v116, v164, -v116
	v_add_f32_e64 v117, v165, -v117
	v_cvt_pk_bf16_f32 v114, v114, v115
	v_cvt_pk_bf16_f32 v115, v116, v117
	v_mfma_f32_16x16x32_bf16 v[78:81], v[14:17], v[74:77], v[78:81]
	v_lshlrev_b32_e32 v116, 16, v76
	v_and_b32_e32 v117, 0xffff0000, v76
	v_lshlrev_b32_e32 v158, 16, v77
	v_and_b32_e32 v159, 0xffff0000, v77
	v_pk_add_f32 v[116:117], v[166:167], v[116:117] neg_lo:[0,1] neg_hi:[0,1]
	v_mfma_f32_16x16x32_bf16 v[118:121], v[54:57], v[74:77], v[118:121]
	v_add_f32_e64 v158, v168, -v158
	v_add_f32_e64 v159, v169, -v159
	v_cvt_pk_bf16_f32 v116, v116, v117
	v_cvt_pk_bf16_f32 v117, v158, v159
	s_waitcnt lgkmcnt(5)
	v_cvt_pk_bf16_f32 v158, v170, v171
	v_mfma_f32_16x16x32_bf16 v[154:157], v[74:77], v[74:77], 0
	v_lshlrev_b32_e32 v160, 16, v158
	v_and_b32_e32 v161, 0xffff0000, v158
	v_cvt_pk_bf16_f32 v159, v172, v173
	v_mfma_f32_16x16x32_bf16 v[78:81], v[6:9], v[114:117], v[78:81]
	v_mfma_f32_16x16x32_bf16 v[74:77], v[74:77], v[114:117], 0
	v_mfma_f32_16x16x32_bf16 v[114:117], v[50:53], v[114:117], v[118:121]
	s_nop 2
	v_add_f32_e64 v118, v170, -v160
	v_add_f32_e64 v119, v171, -v161
	s_waitcnt lgkmcnt(4)
	v_cvt_pk_bf16_f32 v160, v174, v175
	v_cvt_pk_bf16_f32 v161, v176, v177
	v_lshlrev_b32_e32 v120, 16, v159
	v_and_b32_e32 v121, 0xffff0000, v159
	v_mfma_f32_16x16x32_bf16 v[78:81], v[2:5], v[158:161], v[78:81]
	v_add_f32_e64 v120, v172, -v120
	v_add_f32_e64 v121, v173, -v121
	v_cvt_pk_bf16_f32 v118, v118, v119
	v_cvt_pk_bf16_f32 v119, v120, v121
	v_lshlrev_b32_e32 v120, 16, v160
	v_and_b32_e32 v121, 0xffff0000, v160
	v_lshlrev_b32_e32 v162, 16, v161
	v_and_b32_e32 v163, 0xffff0000, v161
	v_mfma_f32_16x16x32_bf16 v[114:117], v[42:45], v[158:161], v[114:117]
	v_add_f32_e64 v120, v174, -v120
	v_add_f32_e64 v121, v175, -v121
	v_pk_add_f32 v[162:163], v[176:177], v[162:163] neg_lo:[0,1] neg_hi:[0,1]
	v_cvt_pk_bf16_f32 v120, v120, v121
	v_cvt_pk_bf16_f32 v121, v162, v163
	v_mfma_f32_16x16x32_bf16 v[154:157], v[158:161], v[158:161], v[154:157]
	v_mfma_f32_16x16x32_bf16 v[78:81], v[10:13], v[158:161], v[78:81]
	v_mfma_f32_16x16x32_bf16 v[74:77], v[158:161], v[118:121], v[74:77]
	v_mfma_f32_16x16x32_bf16 v[114:117], v[46:49], v[158:161], v[114:117]
	v_or_b32_e32 v158, 0x90, v199
	v_cndmask_b32_e64 v159, v196, v158, s[6:7]
	s_nop 4
	v_pk_fma_f32 v[156:157], v[76:77], 2.0, v[156:157] op_sel_hi:[1,0,1]
	v_pk_fma_f32 v[154:155], v[74:75], 2.0, v[154:155] op_sel_hi:[1,0,1]
	v_mfma_f32_16x16x32_bf16 v[74:77], v[2:5], v[118:121], v[78:81]
	s_nop 2
	v_lshl_or_b32 v78, v159, 2, v198
	ds_write_b32 v78, v154
	v_cndmask_b32_e64 v154, v196, v158, s[4:5]
	v_mfma_f32_16x16x32_bf16 v[78:81], v[42:45], v[118:121], v[114:117]
	s_nop 2
	v_lshl_or_b32 v114, v154, 2, v198
	ds_write_b32 v114, v155
	v_cndmask_b32_e64 v114, v196, v158, s[2:3]
	v_lshl_or_b32 v114, v114, 2, v198
	ds_write_b32 v114, v156
	v_cndmask_b32_e32 v114, v196, v158, vcc
	v_lshl_or_b32 v114, v114, 2, v198
	ds_write_b32 v114, v157
	ds_read_b128 v[162:165], v197
	ds_read_b128 v[166:169], v197 offset:64
	ds_read_b128 v[170:173], v197 offset:128
	ds_read_b128 v[174:177], v197 offset:192
	s_mov_b32 s18, 0x7d0000
	buffer_load_dwordx4 v[106:109], v201, s[8:11], s18 offen nt
	s_mov_b32 s18, 0x7d0100
	buffer_load_dwordx4 v[114:117], v201, s[8:11], s18 offen nt
	s_mov_b32 s18, 0x84d000
	buffer_load_dwordx4 v[110:113], v201, s[8:11], s18 offen nt
	s_mov_b32 s18, 0x84d100
	buffer_load_dwordx4 v[118:121], v201, s[8:11], s18 offen nt
	s_mov_b32 s18, 0x8ca000
	buffer_load_dwordx4 v[146:149], v201, s[8:11], s18 offen nt
	s_mov_b32 s18, 0x8ca100
	buffer_load_dwordx4 v[154:157], v201, s[8:11], s18 offen nt
	s_mov_b32 s18, 0x947000
	buffer_load_dwordx4 v[150:153], v201, s[8:11], s18 offen nt
	s_mov_b32 s18, 0x947100
	buffer_load_dwordx4 v[158:161], v201, s[8:11], s18 offen nt
	s_waitcnt vmcnt(22)
	ds_write_b128 v200, v[82:85] offset:4608
	s_waitcnt vmcnt(20)
	ds_write_b128 v200, v[86:89] offset:5760
	s_waitcnt vmcnt(18)
	ds_write_b128 v200, v[122:125] offset:6912
	s_waitcnt vmcnt(16)
	ds_write_b128 v200, v[126:129] offset:8064
	s_waitcnt lgkmcnt(7)
	v_cvt_pk_bf16_f32 v82, v162, v163
	v_cvt_pk_bf16_f32 v83, v164, v165
	s_waitcnt lgkmcnt(6)
	v_cvt_pk_bf16_f32 v84, v166, v167
	v_cvt_pk_bf16_f32 v85, v168, v169
	v_lshlrev_b32_e32 v122, 16, v82
	v_and_b32_e32 v123, 0xffff0000, v82
	v_mfma_f32_16x16x32_bf16 v[86:89], v[22:25], v[82:85], 0
	v_lshlrev_b32_e32 v124, 16, v83
	v_and_b32_e32 v125, 0xffff0000, v83
	v_pk_add_f32 v[122:123], v[162:163], v[122:123] neg_lo:[0,1] neg_hi:[0,1]
	v_mfma_f32_16x16x32_bf16 v[126:129], v[34:37], v[82:85], 0
	v_add_f32_e64 v124, v164, -v124
	v_add_f32_e64 v125, v165, -v125
	v_cvt_pk_bf16_f32 v122, v122, v123
	v_cvt_pk_bf16_f32 v123, v124, v125
	v_lshlrev_b32_e32 v124, 16, v84
	v_and_b32_e32 v125, 0xffff0000, v84
	v_mfma_f32_16x16x32_bf16 v[86:89], v[30:33], v[82:85], v[86:89]
	v_add_f32_e64 v124, v166, -v124
	v_add_f32_e64 v125, v167, -v125
	v_lshlrev_b32_e32 v166, 16, v85
	v_and_b32_e32 v167, 0xffff0000, v85
	v_mfma_f32_16x16x32_bf16 v[126:129], v[38:41], v[82:85], v[126:129]
	v_add_f32_e64 v166, v168, -v166
	v_add_f32_e64 v167, v169, -v167
	v_cvt_pk_bf16_f32 v124, v124, v125
	v_cvt_pk_bf16_f32 v125, v166, v167
	s_waitcnt lgkmcnt(5)
	v_cvt_pk_bf16_f32 v166, v170, v171
	v_mfma_f32_16x16x32_bf16 v[162:165], v[82:85], v[82:85], 0
	v_lshlrev_b32_e32 v168, 16, v166
	v_and_b32_e32 v169, 0xffff0000, v166
	v_cvt_pk_bf16_f32 v167, v172, v173
	v_mfma_f32_16x16x32_bf16 v[86:89], v[22:25], v[122:125], v[86:89]
	v_mfma_f32_16x16x32_bf16 v[82:85], v[82:85], v[122:125], 0
	v_mfma_f32_16x16x32_bf16 v[122:125], v[34:37], v[122:125], v[126:129]
	s_nop 2
	v_add_f32_e64 v126, v170, -v168
	v_add_f32_e64 v127, v171, -v169
	s_waitcnt lgkmcnt(4)
	v_cvt_pk_bf16_f32 v168, v174, v175
	v_cvt_pk_bf16_f32 v169, v176, v177
	v_lshlrev_b32_e32 v128, 16, v167
	v_and_b32_e32 v129, 0xffff0000, v167
	v_mfma_f32_16x16x32_bf16 v[86:89], v[18:21], v[166:169], v[86:89]
	v_add_f32_e64 v128, v172, -v128
	v_add_f32_e64 v129, v173, -v129
	v_cvt_pk_bf16_f32 v126, v126, v127
	v_cvt_pk_bf16_f32 v127, v128, v129
	v_lshlrev_b32_e32 v128, 16, v168
	v_and_b32_e32 v129, 0xffff0000, v168
	v_lshlrev_b32_e32 v170, 16, v169
	v_and_b32_e32 v171, 0xffff0000, v169
	v_mfma_f32_16x16x32_bf16 v[122:125], v[66:69], v[166:169], v[122:125]
	v_add_f32_e64 v128, v174, -v128
	v_add_f32_e64 v129, v175, -v129
	v_pk_add_f32 v[170:171], v[176:177], v[170:171] neg_lo:[0,1] neg_hi:[0,1]
	v_cvt_pk_bf16_f32 v128, v128, v129
	v_cvt_pk_bf16_f32 v129, v170, v171
	v_mfma_f32_16x16x32_bf16 v[162:165], v[166:169], v[166:169], v[162:165]
	v_mfma_f32_16x16x32_bf16 v[86:89], v[26:29], v[166:169], v[86:89]
	v_mfma_f32_16x16x32_bf16 v[82:85], v[166:169], v[126:129], v[82:85]
	v_mfma_f32_16x16x32_bf16 v[122:125], v[70:73], v[166:169], v[122:125]
	v_or_b32_e32 v166, 32, v199
	v_cndmask_b32_e64 v167, v196, v166, s[6:7]
	s_nop 4
	v_pk_fma_f32 v[164:165], v[84:85], 2.0, v[164:165] op_sel_hi:[1,0,1]
	v_pk_fma_f32 v[162:163], v[82:83], 2.0, v[162:163] op_sel_hi:[1,0,1]
	v_mfma_f32_16x16x32_bf16 v[82:85], v[18:21], v[126:129], v[86:89]
	s_nop 2
	v_lshl_or_b32 v86, v167, 2, v198
	ds_write_b32 v86, v162
	v_cndmask_b32_e64 v162, v196, v166, s[4:5]
	v_mfma_f32_16x16x32_bf16 v[86:89], v[66:69], v[126:129], v[122:125]
	s_nop 2
	v_lshl_or_b32 v122, v162, 2, v198
	ds_write_b32 v122, v163
	v_cndmask_b32_e64 v122, v196, v166, s[2:3]
	v_lshl_or_b32 v122, v122, 2, v198
	ds_write_b32 v122, v164
	v_cndmask_b32_e32 v122, v196, v166, vcc
	v_lshl_or_b32 v122, v122, 2, v198
	ds_write_b32 v122, v165
	ds_read_b128 v[170:173], v197 offset:4608
	ds_read_b128 v[174:177], v197 offset:4672
	ds_read_b128 v[178:181], v197 offset:4736
	ds_read_b128 v[182:185], v197 offset:4800
	s_waitcnt vmcnt(15)
	ds_write_b128 v200, v[90:93]
	s_waitcnt vmcnt(13)
	ds_write_b128 v200, v[94:97] offset:1152
	s_waitcnt vmcnt(11)
	ds_write_b128 v200, v[130:133] offset:2304
	s_waitcnt vmcnt(9)
	ds_write_b128 v200, v[134:137] offset:3456
	s_waitcnt lgkmcnt(7)
	v_cvt_pk_bf16_f32 v90, v170, v171
	v_cvt_pk_bf16_f32 v91, v172, v173
	s_waitcnt lgkmcnt(6)
	v_cvt_pk_bf16_f32 v92, v174, v175
	v_cvt_pk_bf16_f32 v93, v176, v177
	v_lshlrev_b32_e32 v94, 16, v90
	v_and_b32_e32 v95, 0xffff0000, v90
	v_mfma_f32_16x16x32_bf16 v[82:85], v[6:9], v[90:93], v[82:85]
	v_lshlrev_b32_e32 v96, 16, v91
	v_and_b32_e32 v97, 0xffff0000, v91
	v_pk_add_f32 v[94:95], v[170:171], v[94:95] neg_lo:[0,1] neg_hi:[0,1]
	v_mfma_f32_16x16x32_bf16 v[86:89], v[50:53], v[90:93], v[86:89]
	v_add_f32_e64 v96, v172, -v96
	v_add_f32_e64 v97, v173, -v97
	v_cvt_pk_bf16_f32 v94, v94, v95
	v_cvt_pk_bf16_f32 v95, v96, v97
	v_lshlrev_b32_e32 v96, 16, v92
	v_and_b32_e32 v97, 0xffff0000, v92
	v_mfma_f32_16x16x32_bf16 v[82:85], v[14:17], v[90:93], v[82:85]
	v_lshlrev_b32_e32 v134, 16, v93
	v_and_b32_e32 v135, 0xffff0000, v93
	v_pk_add_f32 v[96:97], v[174:175], v[96:97] neg_lo:[0,1] neg_hi:[0,1]
	v_mfma_f32_16x16x32_bf16 v[86:89], v[54:57], v[90:93], v[86:89]
	v_add_f32_e64 v134, v176, -v134
	v_add_f32_e64 v135, v177, -v135
	v_cvt_pk_bf16_f32 v96, v96, v97
	v_cvt_pk_bf16_f32 v97, v134, v135
	s_waitcnt lgkmcnt(5)
	v_cvt_pk_bf16_f32 v134, v178, v179
	v_lshlrev_b32_e32 v136, 16, v134
	v_and_b32_e32 v137, 0xffff0000, v134
	v_cvt_pk_bf16_f32 v135, v180, v181
	v_mfma_f32_16x16x32_bf16 v[130:133], v[90:93], v[90:93], 0
	v_mfma_f32_16x16x32_bf16 v[90:93], v[90:93], v[94:97], 0
	v_mfma_f32_16x16x32_bf16 v[82:85], v[6:9], v[94:97], v[82:85]
	v_mfma_f32_16x16x32_bf16 v[86:89], v[50:53], v[94:97], v[86:89]
	v_add_f32_e64 v94, v178, -v136
	v_add_f32_e64 v95, v179, -v137
	s_waitcnt lgkmcnt(4)
	v_cvt_pk_bf16_f32 v136, v182, v183
	v_cvt_pk_bf16_f32 v137, v184, v185
	v_lshlrev_b32_e32 v96, 16, v135
	v_and_b32_e32 v97, 0xffff0000, v135
	v_pk_add_f32 v[96:97], v[180:181], v[96:97] neg_lo:[0,1] neg_hi:[0,1]
	v_cvt_pk_bf16_f32 v94, v94, v95
	v_cvt_pk_bf16_f32 v95, v96, v97
	v_lshlrev_b32_e32 v96, 16, v136
	v_and_b32_e32 v97, 0xffff0000, v136
	v_lshlrev_b32_e32 v170, 16, v137
	v_and_b32_e32 v171, 0xffff0000, v137
	v_pk_add_f32 v[96:97], v[182:183], v[96:97] neg_lo:[0,1] neg_hi:[0,1]
	v_pk_add_f32 v[170:171], v[184:185], v[170:171] neg_lo:[0,1] neg_hi:[0,1]
	v_cvt_pk_bf16_f32 v96, v96, v97
	v_cvt_pk_bf16_f32 v97, v170, v171
	v_mfma_f32_16x16x32_bf16 v[130:133], v[134:137], v[134:137], v[130:133]
	s_nop 0
	v_mfma_f32_16x16x32_bf16 v[90:93], v[134:137], v[94:97], v[90:93]
	v_mfma_f32_16x16x32_bf16 v[82:85], v[2:5], v[134:137], v[82:85]
	v_mfma_f32_16x16x32_bf16 v[86:89], v[42:45], v[134:137], v[86:89]
	s_nop 5
	v_fma_f32 v90, v90, 2.0, v130
	v_fma_f32 v91, v91, 2.0, v131
	v_or_b32_e32 v130, 0xa0, v199
	v_cndmask_b32_e64 v131, v196, v130, s[6:7]
	v_mfma_f32_16x16x32_bf16 v[82:85], v[10:13], v[134:137], v[82:85]
	v_lshl_or_b32 v131, v131, 2, v198
	ds_write_b32 v131, v90
	v_cndmask_b32_e64 v90, v196, v130, s[4:5]
	v_mfma_f32_16x16x32_bf16 v[86:89], v[46:49], v[134:137], v[86:89]
	v_lshl_or_b32 v90, v90, 2, v198
	ds_write_b32 v90, v91
	v_cndmask_b32_e64 v90, v196, v130, s[2:3]
	v_mfma_f32_16x16x32_bf16 v[82:85], v[2:5], v[94:97], v[82:85]
	v_fma_f32 v92, v92, 2.0, v132
	v_fma_f32 v93, v93, 2.0, v133
	v_lshl_or_b32 v90, v90, 2, v198
	ds_write_b32 v90, v92
	v_mfma_f32_16x16x32_bf16 v[86:89], v[42:45], v[94:97], v[86:89]
	v_cndmask_b32_e32 v90, v196, v130, vcc
	v_lshl_or_b32 v90, v90, 2, v198
	ds_write_b32 v90, v93
	ds_read_b128 v[90:93], v197
	ds_read_b128 v[94:97], v197 offset:64
	ds_read_b128 v[178:181], v197 offset:128
	ds_read_b128 v[182:185], v197 offset:192
	s_mov_b32 s18, 0x9c4000
	buffer_load_dwordx4 v[122:125], v201, s[8:11], s18 offen nt
	s_mov_b32 s18, 0x9c4100
	buffer_load_dwordx4 v[130:133], v201, s[8:11], s18 offen nt
	s_mov_b32 s18, 0xa41000
	buffer_load_dwordx4 v[126:129], v201, s[8:11], s18 offen nt
	s_mov_b32 s18, 0xa41100
	buffer_load_dwordx4 v[134:137], v201, s[8:11], s18 offen nt
	s_mov_b32 s18, 0xabe000
	buffer_load_dwordx4 v[162:165], v201, s[8:11], s18 offen nt
	s_mov_b32 s18, 0xabe100
	buffer_load_dwordx4 v[170:173], v201, s[8:11], s18 offen nt
	s_mov_b32 s18, 0xb3b000
	buffer_load_dwordx4 v[166:169], v201, s[8:11], s18 offen nt
	s_mov_b32 s18, 0xb3b100
	buffer_load_dwordx4 v[174:177], v201, s[8:11], s18 offen nt
	s_waitcnt vmcnt(22)
	ds_write_b128 v200, v[98:101] offset:4608
	s_waitcnt vmcnt(20)
	ds_write_b128 v200, v[102:105] offset:5760
	s_waitcnt vmcnt(18)
	ds_write_b128 v200, v[138:141] offset:6912
	s_waitcnt vmcnt(16)
	ds_write_b128 v200, v[142:145] offset:8064
	s_waitcnt lgkmcnt(7)
	v_cvt_pk_bf16_f32 v98, v90, v91
	v_cvt_pk_bf16_f32 v99, v92, v93
	s_waitcnt lgkmcnt(6)
	v_cvt_pk_bf16_f32 v100, v94, v95
	v_cvt_pk_bf16_f32 v101, v96, v97
	v_lshlrev_b32_e32 v138, 16, v98
	v_and_b32_e32 v139, 0xffff0000, v98
	v_mfma_f32_16x16x32_bf16 v[102:105], v[22:25], v[98:101], 0
	v_add_f32_e64 v90, v90, -v138
	v_add_f32_e64 v91, v91, -v139
	v_lshlrev_b32_e32 v142, 16, v99
	v_and_b32_e32 v143, 0xffff0000, v99
	v_mfma_f32_16x16x32_bf16 v[138:141], v[34:37], v[98:101], 0
	v_add_f32_e64 v92, v92, -v142
	v_add_f32_e64 v93, v93, -v143
	v_cvt_pk_bf16_f32 v90, v90, v91
	v_cvt_pk_bf16_f32 v91, v92, v93
	v_lshlrev_b32_e32 v92, 16, v100
	v_and_b32_e32 v93, 0xffff0000, v100
	v_mfma_f32_16x16x32_bf16 v[102:105], v[30:33], v[98:101], v[102:105]
	v_add_f32_e64 v92, v94, -v92
	v_add_f32_e64 v93, v95, -v93
	v_lshlrev_b32_e32 v94, 16, v101
	v_and_b32_e32 v95, 0xffff0000, v101
	v_mfma_f32_16x16x32_bf16 v[138:141], v[38:41], v[98:101], v[138:141]
	v_add_f32_e64 v94, v96, -v94
	v_add_f32_e64 v95, v97, -v95
	v_cvt_pk_bf16_f32 v92, v92, v93
	v_cvt_pk_bf16_f32 v93, v94, v95
	v_mfma_f32_16x16x32_bf16 v[142:145], v[98:101], v[98:101], 0
	s_nop 0
	v_mfma_f32_16x16x32_bf16 v[94:97], v[98:101], v[90:93], 0
	v_mfma_f32_16x16x32_bf16 v[98:101], v[22:25], v[90:93], v[102:105]
	s_waitcnt lgkmcnt(5)
	s_nop 1
	v_cvt_pk_bf16_f32 v102, v178, v179
	v_lshlrev_b32_e32 v104, 16, v102
	v_and_b32_e32 v105, 0xffff0000, v102
	v_mfma_f32_16x16x32_bf16 v[90:93], v[34:37], v[90:93], v[138:141]
	v_add_f32_e64 v104, v178, -v104
	v_add_f32_e64 v105, v179, -v105
	v_cvt_pk_bf16_f32 v103, v180, v181
	v_cvt_pk_bf16_f32 v138, v104, v105
	s_waitcnt lgkmcnt(4)
	v_cvt_pk_bf16_f32 v104, v182, v183
	v_cvt_pk_bf16_f32 v105, v184, v185
	v_lshlrev_b32_e32 v140, 16, v103
	v_and_b32_e32 v141, 0xffff0000, v103
	v_mfma_f32_16x16x32_bf16 v[98:101], v[18:21], v[102:105], v[98:101]
	v_add_f32_e64 v140, v180, -v140
	v_add_f32_e64 v141, v181, -v141
	v_lshlrev_b32_e32 v178, 16, v105
	v_cvt_pk_bf16_f32 v139, v140, v141
	v_lshlrev_b32_e32 v140, 16, v104
	v_and_b32_e32 v141, 0xffff0000, v104
	v_and_b32_e32 v179, 0xffff0000, v105
	v_mfma_f32_16x16x32_bf16 v[90:93], v[66:69], v[102:105], v[90:93]
	v_add_f32_e64 v140, v182, -v140
	v_add_f32_e64 v141, v183, -v141
	v_pk_add_f32 v[178:179], v[184:185], v[178:179] neg_lo:[0,1] neg_hi:[0,1]
	v_cvt_pk_bf16_f32 v140, v140, v141
	v_cvt_pk_bf16_f32 v141, v178, v179
	v_mfma_f32_16x16x32_bf16 v[142:145], v[102:105], v[102:105], v[142:145]
	v_mfma_f32_16x16x32_bf16 v[98:101], v[26:29], v[102:105], v[98:101]
	v_mfma_f32_16x16x32_bf16 v[94:97], v[102:105], v[138:141], v[94:97]
	v_mfma_f32_16x16x32_bf16 v[90:93], v[70:73], v[102:105], v[90:93]
	v_or_b32_e32 v104, 48, v199
	v_cndmask_b32_e64 v105, v196, v104, s[6:7]
	s_nop 4
	v_pk_fma_f32 v[144:145], v[96:97], 2.0, v[144:145] op_sel_hi:[1,0,1]
	v_pk_fma_f32 v[102:103], v[94:95], 2.0, v[142:143] op_sel_hi:[1,0,1]
	v_mfma_f32_16x16x32_bf16 v[94:97], v[18:21], v[138:141], v[98:101]
	s_nop 2
	v_lshl_or_b32 v98, v105, 2, v198
	ds_write_b32 v98, v102
	v_cndmask_b32_e64 v98, v196, v104, s[4:5]
	v_lshl_or_b32 v98, v98, 2, v198
	v_mfma_f32_16x16x32_bf16 v[90:93], v[66:69], v[138:141], v[90:93]
	ds_write_b32 v98, v103
	v_cndmask_b32_e64 v98, v196, v104, s[2:3]
	v_lshl_or_b32 v98, v98, 2, v198
	ds_write_b32 v98, v144
	v_cndmask_b32_e32 v98, v196, v104, vcc
	v_lshl_or_b32 v98, v98, 2, v198
	ds_write_b32 v98, v145
	ds_read_b128 v[98:101], v197 offset:4608
	ds_read_b128 v[102:105], v197 offset:4672
	ds_read_b128 v[186:189], v197 offset:4736
	ds_read_b128 v[190:193], v197 offset:4800
	s_waitcnt vmcnt(15)
	ds_write_b128 v200, v[106:109]
	s_waitcnt vmcnt(13)
	ds_write_b128 v200, v[110:113] offset:1152
	s_waitcnt vmcnt(11)
	ds_write_b128 v200, v[146:149] offset:2304
	s_waitcnt vmcnt(9)
	ds_write_b128 v200, v[150:153] offset:3456
	s_waitcnt lgkmcnt(7)
	v_cvt_pk_bf16_f32 v106, v98, v99
	v_cvt_pk_bf16_f32 v107, v100, v101
	s_waitcnt lgkmcnt(6)
	v_cvt_pk_bf16_f32 v108, v102, v103
	v_cvt_pk_bf16_f32 v109, v104, v105
	v_lshlrev_b32_e32 v110, 16, v106
	v_and_b32_e32 v111, 0xffff0000, v106
	v_mfma_f32_16x16x32_bf16 v[94:97], v[6:9], v[106:109], v[94:97]
	v_add_f32_e64 v98, v98, -v110
	v_add_f32_e64 v99, v99, -v111
	v_lshlrev_b32_e32 v110, 16, v107
	v_and_b32_e32 v111, 0xffff0000, v107
	v_mfma_f32_16x16x32_bf16 v[90:93], v[50:53], v[106:109], v[90:93]
	v_add_f32_e64 v100, v100, -v110
	v_add_f32_e64 v101, v101, -v111
	v_cvt_pk_bf16_f32 v98, v98, v99
	v_cvt_pk_bf16_f32 v99, v100, v101
	v_lshlrev_b32_e32 v100, 16, v108
	v_and_b32_e32 v101, 0xffff0000, v108
	v_mfma_f32_16x16x32_bf16 v[94:97], v[14:17], v[106:109], v[94:97]
	v_add_f32_e64 v100, v102, -v100
	v_add_f32_e64 v101, v103, -v101
	v_lshlrev_b32_e32 v102, 16, v109
	v_and_b32_e32 v103, 0xffff0000, v109
	v_mfma_f32_16x16x32_bf16 v[90:93], v[54:57], v[106:109], v[90:93]
	v_add_f32_e64 v102, v104, -v102
	v_add_f32_e64 v103, v105, -v103
	v_cvt_pk_bf16_f32 v100, v100, v101
	v_cvt_pk_bf16_f32 v101, v102, v103
	v_mfma_f32_16x16x32_bf16 v[110:113], v[106:109], v[106:109], 0
	s_nop 0
	v_mfma_f32_16x16x32_bf16 v[102:105], v[106:109], v[98:101], 0
	s_waitcnt lgkmcnt(5)
	v_cvt_pk_bf16_f32 v106, v186, v187
	v_lshlrev_b32_e32 v108, 16, v106
	v_and_b32_e32 v109, 0xffff0000, v106
	v_mfma_f32_16x16x32_bf16 v[94:97], v[6:9], v[98:101], v[94:97]
	v_cvt_pk_bf16_f32 v107, v188, v189
	v_mfma_f32_16x16x32_bf16 v[90:93], v[50:53], v[98:101], v[90:93]
	v_add_f32_e64 v98, v186, -v108
	v_add_f32_e64 v99, v187, -v109
	s_waitcnt lgkmcnt(4)
	v_cvt_pk_bf16_f32 v108, v190, v191
	v_cvt_pk_bf16_f32 v109, v192, v193
	v_lshlrev_b32_e32 v100, 16, v107
	v_and_b32_e32 v101, 0xffff0000, v107
	v_pk_add_f32 v[100:101], v[188:189], v[100:101] neg_lo:[0,1] neg_hi:[0,1]
	v_cvt_pk_bf16_f32 v98, v98, v99
	v_cvt_pk_bf16_f32 v99, v100, v101
	v_lshlrev_b32_e32 v100, 16, v108
	v_and_b32_e32 v101, 0xffff0000, v108
	v_lshlrev_b32_e32 v146, 16, v109
	v_and_b32_e32 v147, 0xffff0000, v109
	v_mfma_f32_16x16x32_bf16 v[94:97], v[2:5], v[106:109], v[94:97]
	v_add_f32_e64 v100, v190, -v100
	v_add_f32_e64 v101, v191, -v101
	v_pk_add_f32 v[146:147], v[192:193], v[146:147] neg_lo:[0,1] neg_hi:[0,1]
	v_cvt_pk_bf16_f32 v100, v100, v101
	v_cvt_pk_bf16_f32 v101, v146, v147
	v_mfma_f32_16x16x32_bf16 v[90:93], v[42:45], v[106:109], v[90:93]
	v_mfma_f32_16x16x32_bf16 v[110:113], v[106:109], v[106:109], v[110:113]
	v_mfma_f32_16x16x32_bf16 v[102:105], v[106:109], v[98:101], v[102:105]
	v_mfma_f32_16x16x32_bf16 v[94:97], v[10:13], v[106:109], v[94:97]
	s_nop 6
	v_fma_f32 v112, v104, 2.0, v112
	v_fma_f32 v113, v105, 2.0, v113
	v_mfma_f32_16x16x32_bf16 v[104:107], v[46:49], v[106:109], v[90:93]
	v_or_b32_e32 v108, 0xb0, v199
	v_cndmask_b32_e64 v109, v196, v108, s[6:7]
	v_pk_fma_f32 v[102:103], v[102:103], 2.0, v[110:111] op_sel_hi:[1,0,1]
	v_mfma_f32_16x16x32_bf16 v[90:93], v[2:5], v[98:101], v[94:97]
	s_nop 2
	v_lshl_or_b32 v94, v109, 2, v198
	ds_write_b32 v94, v102
	v_cndmask_b32_e64 v102, v196, v108, s[4:5]
	v_mfma_f32_16x16x32_bf16 v[94:97], v[42:45], v[98:101], v[104:107]
	v_lshl_or_b32 v98, v102, 2, v198
	ds_write_b32 v98, v103
	v_cndmask_b32_e64 v98, v196, v108, s[2:3]
	v_lshl_or_b32 v98, v98, 2, v198
	ds_write_b32 v98, v112
	v_cndmask_b32_e32 v98, v196, v108, vcc
	v_lshl_or_b32 v98, v98, 2, v198
	ds_write_b32 v98, v113
	ds_read_b128 v[98:101], v197
	ds_read_b128 v[102:105], v197 offset:64
	ds_read_b128 v[106:109], v197 offset:128
	ds_read_b128 v[110:113], v197 offset:192
	s_mov_b32 s18, 0xbb8000
	buffer_load_dwordx4 v[138:141], v201, s[8:11], s18 offen nt
	s_mov_b32 s18, 0xbb8100
	buffer_load_dwordx4 v[146:149], v201, s[8:11], s18 offen nt
	s_mov_b32 s18, 0xc35000
	buffer_load_dwordx4 v[142:145], v201, s[8:11], s18 offen nt
	s_mov_b32 s18, 0xc35100
	buffer_load_dwordx4 v[150:153], v201, s[8:11], s18 offen nt
	s_mov_b32 s18, 0xcb2000
	buffer_load_dwordx4 v[178:181], v201, s[8:11], s18 offen nt
	s_mov_b32 s18, 0xcb2100
	buffer_load_dwordx4 v[186:189], v201, s[8:11], s18 offen nt
	s_mov_b32 s18, 0xd2f000
	buffer_load_dwordx4 v[182:185], v201, s[8:11], s18 offen nt
	s_mov_b32 s18, 0xd2f100
	buffer_load_dwordx4 v[190:193], v201, s[8:11], s18 offen nt
	s_waitcnt vmcnt(22)
	ds_write_b128 v200, v[114:117] offset:4608
	s_waitcnt vmcnt(20)
	ds_write_b128 v200, v[118:121] offset:5760
	s_waitcnt vmcnt(18)
	ds_write_b128 v200, v[154:157] offset:6912
	s_waitcnt vmcnt(16)
	ds_write_b128 v200, v[158:161] offset:8064
	s_waitcnt lgkmcnt(7)
	v_cvt_pk_bf16_f32 v114, v98, v99
	v_cvt_pk_bf16_f32 v115, v100, v101
	s_waitcnt lgkmcnt(6)
	v_cvt_pk_bf16_f32 v116, v102, v103
	v_cvt_pk_bf16_f32 v117, v104, v105
	v_lshlrev_b32_e32 v154, 16, v114
	v_and_b32_e32 v155, 0xffff0000, v114
	v_mfma_f32_16x16x32_bf16 v[118:121], v[22:25], v[114:117], 0
	v_add_f32_e64 v98, v98, -v154
	v_add_f32_e64 v99, v99, -v155
	v_lshlrev_b32_e32 v158, 16, v115
	v_and_b32_e32 v159, 0xffff0000, v115
	v_mfma_f32_16x16x32_bf16 v[154:157], v[34:37], v[114:117], 0
	v_add_f32_e64 v100, v100, -v158
	v_add_f32_e64 v101, v101, -v159
	v_cvt_pk_bf16_f32 v98, v98, v99
	v_cvt_pk_bf16_f32 v99, v100, v101
	v_lshlrev_b32_e32 v100, 16, v116
	v_and_b32_e32 v101, 0xffff0000, v116
	v_mfma_f32_16x16x32_bf16 v[118:121], v[30:33], v[114:117], v[118:121]
	v_add_f32_e64 v100, v102, -v100
	v_add_f32_e64 v101, v103, -v101
	v_lshlrev_b32_e32 v102, 16, v117
	v_and_b32_e32 v103, 0xffff0000, v117
	v_mfma_f32_16x16x32_bf16 v[154:157], v[38:41], v[114:117], v[154:157]
	v_add_f32_e64 v102, v104, -v102
	v_add_f32_e64 v103, v105, -v103
	v_cvt_pk_bf16_f32 v100, v100, v101
	v_cvt_pk_bf16_f32 v101, v102, v103
	v_mfma_f32_16x16x32_bf16 v[158:161], v[114:117], v[114:117], 0
	s_nop 0
	v_mfma_f32_16x16x32_bf16 v[102:105], v[114:117], v[98:101], 0
	v_mfma_f32_16x16x32_bf16 v[114:117], v[22:25], v[98:101], v[118:121]
	s_waitcnt lgkmcnt(5)
	s_nop 1
	v_cvt_pk_bf16_f32 v118, v106, v107
	v_cvt_pk_bf16_f32 v119, v108, v109
	v_lshlrev_b32_e32 v120, 16, v118
	v_and_b32_e32 v121, 0xffff0000, v118
	v_mfma_f32_16x16x32_bf16 v[98:101], v[34:37], v[98:101], v[154:157]
	v_add_f32_e64 v106, v106, -v120
	v_add_f32_e64 v107, v107, -v121
	s_waitcnt lgkmcnt(4)
	v_cvt_pk_bf16_f32 v120, v110, v111
	v_cvt_pk_bf16_f32 v121, v112, v113
	v_lshlrev_b32_e32 v154, 16, v119
	v_and_b32_e32 v155, 0xffff0000, v119
	v_pk_add_f32 v[108:109], v[108:109], v[154:155] neg_lo:[0,1] neg_hi:[0,1]
	v_cvt_pk_bf16_f32 v106, v106, v107
	v_mfma_f32_16x16x32_bf16 v[114:117], v[18:21], v[118:121], v[114:117]
	v_cvt_pk_bf16_f32 v107, v108, v109
	v_lshlrev_b32_e32 v108, 16, v120
	v_and_b32_e32 v109, 0xffff0000, v120
	v_pk_add_f32 v[108:109], v[110:111], v[108:109] neg_lo:[0,1] neg_hi:[0,1]
	v_lshlrev_b32_e32 v110, 16, v121
	v_and_b32_e32 v111, 0xffff0000, v121
	v_mfma_f32_16x16x32_bf16 v[98:101], v[66:69], v[118:121], v[98:101]
	v_add_f32_e64 v110, v112, -v110
	v_add_f32_e64 v111, v113, -v111
	v_cvt_pk_bf16_f32 v108, v108, v109
	v_cvt_pk_bf16_f32 v109, v110, v111
	v_mfma_f32_16x16x32_bf16 v[154:157], v[118:121], v[118:121], v[158:161]
	v_mfma_f32_16x16x32_bf16 v[114:117], v[26:29], v[118:121], v[114:117]
	v_mfma_f32_16x16x32_bf16 v[102:105], v[118:121], v[106:109], v[102:105]
	v_mfma_f32_16x16x32_bf16 v[98:101], v[70:73], v[118:121], v[98:101]
	v_or_b32_e32 v118, 64, v199
	v_cndmask_b32_e64 v119, v196, v118, s[6:7]
	s_nop 4
	v_pk_fma_f32 v[110:111], v[104:105], 2.0, v[156:157] op_sel_hi:[1,0,1]
	v_pk_fma_f32 v[112:113], v[102:103], 2.0, v[154:155] op_sel_hi:[1,0,1]
	v_mfma_f32_16x16x32_bf16 v[102:105], v[18:21], v[106:109], v[114:117]
	s_nop 2
	v_lshl_or_b32 v114, v119, 2, v198
	ds_write_b32 v114, v112
	v_cndmask_b32_e64 v112, v196, v118, s[4:5]
	v_mfma_f32_16x16x32_bf16 v[98:101], v[66:69], v[106:109], v[98:101]
	v_lshl_or_b32 v106, v112, 2, v198
	ds_write_b32 v106, v113
	v_cndmask_b32_e64 v106, v196, v118, s[2:3]
	v_lshl_or_b32 v106, v106, 2, v198
	ds_write_b32 v106, v110
	v_cndmask_b32_e32 v106, v196, v118, vcc
	v_lshl_or_b32 v106, v106, 2, v198
	ds_write_b32 v106, v111
	ds_read_b128 v[106:109], v197 offset:4608
	ds_read_b128 v[110:113], v197 offset:4672
	ds_read_b128 v[202:205], v197 offset:4736
	ds_read_b128 v[206:209], v197 offset:4800
	s_waitcnt vmcnt(15)
	ds_write_b128 v200, v[122:125]
	s_waitcnt vmcnt(13)
	ds_write_b128 v200, v[126:129] offset:1152
	s_waitcnt vmcnt(11)
	ds_write_b128 v200, v[162:165] offset:2304
	s_waitcnt vmcnt(9)
	ds_write_b128 v200, v[166:169] offset:3456
	s_waitcnt lgkmcnt(7)
	v_cvt_pk_bf16_f32 v122, v106, v107
	v_cvt_pk_bf16_f32 v123, v108, v109
	s_waitcnt lgkmcnt(6)
	v_cvt_pk_bf16_f32 v124, v110, v111
	v_cvt_pk_bf16_f32 v125, v112, v113
	v_lshlrev_b32_e32 v126, 16, v122
	v_and_b32_e32 v127, 0xffff0000, v122
	v_mfma_f32_16x16x32_bf16 v[102:105], v[6:9], v[122:125], v[102:105]
	v_add_f32_e64 v106, v106, -v126
	v_add_f32_e64 v107, v107, -v127
	v_lshlrev_b32_e32 v126, 16, v123
	v_and_b32_e32 v127, 0xffff0000, v123
	v_mfma_f32_16x16x32_bf16 v[98:101], v[50:53], v[122:125], v[98:101]
	v_add_f32_e64 v108, v108, -v126
	v_add_f32_e64 v109, v109, -v127
	v_cvt_pk_bf16_f32 v106, v106, v107
	v_cvt_pk_bf16_f32 v107, v108, v109
	v_lshlrev_b32_e32 v108, 16, v124
	v_and_b32_e32 v109, 0xffff0000, v124
	v_mfma_f32_16x16x32_bf16 v[102:105], v[14:17], v[122:125], v[102:105]
	v_add_f32_e64 v108, v110, -v108
	v_add_f32_e64 v109, v111, -v109
	v_lshlrev_b32_e32 v110, 16, v125
	v_and_b32_e32 v111, 0xffff0000, v125
	v_mfma_f32_16x16x32_bf16 v[98:101], v[54:57], v[122:125], v[98:101]
	v_add_f32_e64 v110, v112, -v110
	v_add_f32_e64 v111, v113, -v111
	v_cvt_pk_bf16_f32 v108, v108, v109
	v_cvt_pk_bf16_f32 v109, v110, v111
	v_mfma_f32_16x16x32_bf16 v[126:129], v[122:125], v[122:125], 0
	s_nop 0
	v_mfma_f32_16x16x32_bf16 v[110:113], v[122:125], v[106:109], 0
	s_waitcnt lgkmcnt(5)
	v_cvt_pk_bf16_f32 v122, v202, v203
	v_lshlrev_b32_e32 v124, 16, v122
	v_and_b32_e32 v125, 0xffff0000, v122
	v_mfma_f32_16x16x32_bf16 v[102:105], v[6:9], v[106:109], v[102:105]
	v_cvt_pk_bf16_f32 v123, v204, v205
	v_mfma_f32_16x16x32_bf16 v[98:101], v[50:53], v[106:109], v[98:101]
	v_add_f32_e64 v106, v202, -v124
	v_add_f32_e64 v107, v203, -v125
	s_waitcnt lgkmcnt(4)
	v_cvt_pk_bf16_f32 v124, v206, v207
	v_cvt_pk_bf16_f32 v125, v208, v209
	v_lshlrev_b32_e32 v108, 16, v123
	v_and_b32_e32 v109, 0xffff0000, v123
	v_pk_add_f32 v[108:109], v[204:205], v[108:109] neg_lo:[0,1] neg_hi:[0,1]
	v_cvt_pk_bf16_f32 v106, v106, v107
	v_cvt_pk_bf16_f32 v107, v108, v109
	v_lshlrev_b32_e32 v108, 16, v124
	v_and_b32_e32 v109, 0xffff0000, v124
	v_lshlrev_b32_e32 v162, 16, v125
	v_and_b32_e32 v163, 0xffff0000, v125
	v_mfma_f32_16x16x32_bf16 v[102:105], v[2:5], v[122:125], v[102:105]
	v_add_f32_e64 v108, v206, -v108
	v_add_f32_e64 v109, v207, -v109
	v_pk_add_f32 v[162:163], v[208:209], v[162:163] neg_lo:[0,1] neg_hi:[0,1]
	v_cvt_pk_bf16_f32 v108, v108, v109
	v_cvt_pk_bf16_f32 v109, v162, v163
	v_mfma_f32_16x16x32_bf16 v[98:101], v[42:45], v[122:125], v[98:101]
	v_mfma_f32_16x16x32_bf16 v[126:129], v[122:125], v[122:125], v[126:129]
	v_mfma_f32_16x16x32_bf16 v[110:113], v[122:125], v[106:109], v[110:113]
	v_mfma_f32_16x16x32_bf16 v[102:105], v[10:13], v[122:125], v[102:105]
	v_mfma_f32_16x16x32_bf16 v[122:125], v[46:49], v[122:125], v[98:101]
	s_nop 5
	v_fma_f32 v110, v110, 2.0, v126
	v_fma_f32 v111, v111, 2.0, v127
	v_or_b32_e32 v126, 0xc0, v199
	v_cndmask_b32_e64 v127, v196, v126, s[6:7]
	v_mfma_f32_16x16x32_bf16 v[98:101], v[2:5], v[106:109], v[102:105]
	v_fma_f32 v112, v112, 2.0, v128
	v_fma_f32 v113, v113, 2.0, v129
	s_nop 0
	v_lshl_or_b32 v102, v127, 2, v198
	ds_write_b32 v102, v110
	v_cndmask_b32_e64 v110, v196, v126, s[4:5]
	v_mfma_f32_16x16x32_bf16 v[102:105], v[42:45], v[106:109], v[122:125]
	v_lshl_or_b32 v106, v110, 2, v198
	ds_write_b32 v106, v111
	v_cndmask_b32_e64 v106, v196, v126, s[2:3]
	v_lshl_or_b32 v106, v106, 2, v198
	ds_write_b32 v106, v112
	v_cndmask_b32_e32 v106, v196, v126, vcc
	v_lshl_or_b32 v106, v106, 2, v198
	ds_write_b32 v106, v113
	ds_read_b128 v[106:109], v197
	ds_read_b128 v[110:113], v197 offset:64
	ds_read_b128 v[202:205], v197 offset:128
	ds_read_b128 v[206:209], v197 offset:192
	s_mov_b32 s18, 0xdac000
	buffer_load_dwordx4 v[114:117], v201, s[8:11], s18 offen nt
	s_mov_b32 s18, 0xdac100
	buffer_load_dwordx4 v[122:125], v201, s[8:11], s18 offen nt
	s_mov_b32 s18, 0xe29000
	buffer_load_dwordx4 v[118:121], v201, s[8:11], s18 offen nt
	s_mov_b32 s18, 0xe29100
	buffer_load_dwordx4 v[126:129], v201, s[8:11], s18 offen nt
	s_mov_b32 s18, 0xea6000
	buffer_load_dwordx4 v[154:157], v201, s[8:11], s18 offen nt
	s_mov_b32 s18, 0xea6100
	buffer_load_dwordx4 v[162:165], v201, s[8:11], s18 offen nt
	s_mov_b32 s18, 0xf23000
	buffer_load_dwordx4 v[158:161], v201, s[8:11], s18 offen nt
	s_mov_b32 s18, 0xf23100
	buffer_load_dwordx4 v[166:169], v201, s[8:11], s18 offen nt
	s_waitcnt vmcnt(22)
	ds_write_b128 v200, v[130:133] offset:4608
	s_waitcnt vmcnt(20)
	ds_write_b128 v200, v[134:137] offset:5760
	s_waitcnt vmcnt(18)
	ds_write_b128 v200, v[170:173] offset:6912
	s_waitcnt vmcnt(16)
	ds_write_b128 v200, v[174:177] offset:8064
	s_waitcnt lgkmcnt(7)
	v_cvt_pk_bf16_f32 v130, v106, v107
	v_cvt_pk_bf16_f32 v131, v108, v109
	s_waitcnt lgkmcnt(6)
	v_cvt_pk_bf16_f32 v132, v110, v111
	v_cvt_pk_bf16_f32 v133, v112, v113
	v_lshlrev_b32_e32 v170, 16, v130
	v_and_b32_e32 v171, 0xffff0000, v130
	v_mfma_f32_16x16x32_bf16 v[134:137], v[22:25], v[130:133], 0
	v_add_f32_e64 v106, v106, -v170
	v_add_f32_e64 v107, v107, -v171
	v_lshlrev_b32_e32 v174, 16, v131
	v_and_b32_e32 v175, 0xffff0000, v131
	v_mfma_f32_16x16x32_bf16 v[170:173], v[34:37], v[130:133], 0
	v_add_f32_e64 v108, v108, -v174
	v_add_f32_e64 v109, v109, -v175
	v_cvt_pk_bf16_f32 v106, v106, v107
	v_cvt_pk_bf16_f32 v107, v108, v109
	v_lshlrev_b32_e32 v108, 16, v132
	v_and_b32_e32 v109, 0xffff0000, v132
	v_mfma_f32_16x16x32_bf16 v[134:137], v[30:33], v[130:133], v[134:137]
	v_add_f32_e64 v108, v110, -v108
	v_add_f32_e64 v109, v111, -v109
	v_lshlrev_b32_e32 v110, 16, v133
	v_and_b32_e32 v111, 0xffff0000, v133
	v_mfma_f32_16x16x32_bf16 v[170:173], v[38:41], v[130:133], v[170:173]
	v_add_f32_e64 v110, v112, -v110
	v_add_f32_e64 v111, v113, -v111
	v_cvt_pk_bf16_f32 v108, v108, v109
	v_cvt_pk_bf16_f32 v109, v110, v111
	v_mfma_f32_16x16x32_bf16 v[174:177], v[130:133], v[130:133], 0
	s_nop 0
	v_mfma_f32_16x16x32_bf16 v[110:113], v[130:133], v[106:109], 0
	v_mfma_f32_16x16x32_bf16 v[130:133], v[22:25], v[106:109], v[134:137]
	s_waitcnt lgkmcnt(5)
	s_nop 1
	v_cvt_pk_bf16_f32 v134, v202, v203
	v_lshlrev_b32_e32 v136, 16, v134
	v_and_b32_e32 v137, 0xffff0000, v134
	v_mfma_f32_16x16x32_bf16 v[106:109], v[34:37], v[106:109], v[170:173]
	v_add_f32_e64 v136, v202, -v136
	v_add_f32_e64 v137, v203, -v137
	v_cvt_pk_bf16_f32 v135, v204, v205
	v_cvt_pk_bf16_f32 v170, v136, v137
	s_waitcnt lgkmcnt(4)
	v_cvt_pk_bf16_f32 v136, v206, v207
	v_cvt_pk_bf16_f32 v137, v208, v209
	v_lshlrev_b32_e32 v172, 16, v135
	v_and_b32_e32 v173, 0xffff0000, v135
	v_mfma_f32_16x16x32_bf16 v[130:133], v[18:21], v[134:137], v[130:133]
	v_add_f32_e64 v172, v204, -v172
	v_add_f32_e64 v173, v205, -v173
	v_lshlrev_b32_e32 v202, 16, v137
	v_cvt_pk_bf16_f32 v171, v172, v173
	v_lshlrev_b32_e32 v172, 16, v136
	v_and_b32_e32 v173, 0xffff0000, v136
	v_and_b32_e32 v203, 0xffff0000, v137
	v_mfma_f32_16x16x32_bf16 v[106:109], v[66:69], v[134:137], v[106:109]
	v_add_f32_e64 v172, v206, -v172
	v_add_f32_e64 v173, v207, -v173
	v_pk_add_f32 v[202:203], v[208:209], v[202:203] neg_lo:[0,1] neg_hi:[0,1]
	v_cvt_pk_bf16_f32 v172, v172, v173
	v_cvt_pk_bf16_f32 v173, v202, v203
	v_mfma_f32_16x16x32_bf16 v[174:177], v[134:137], v[134:137], v[174:177]
	v_mfma_f32_16x16x32_bf16 v[130:133], v[26:29], v[134:137], v[130:133]
	v_mfma_f32_16x16x32_bf16 v[110:113], v[134:137], v[170:173], v[110:113]
	v_mfma_f32_16x16x32_bf16 v[106:109], v[70:73], v[134:137], v[106:109]
	v_or_b32_e32 v136, 0x50, v199
	v_cndmask_b32_e64 v137, v196, v136, s[6:7]
	s_nop 4
	v_pk_fma_f32 v[176:177], v[112:113], 2.0, v[176:177] op_sel_hi:[1,0,1]
	v_pk_fma_f32 v[134:135], v[110:111], 2.0, v[174:175] op_sel_hi:[1,0,1]
	v_mfma_f32_16x16x32_bf16 v[110:113], v[18:21], v[170:173], v[130:133]
	s_nop 2
	v_lshl_or_b32 v130, v137, 2, v198
	ds_write_b32 v130, v134
	v_cndmask_b32_e64 v130, v196, v136, s[4:5]
	v_lshl_or_b32 v130, v130, 2, v198
	v_mfma_f32_16x16x32_bf16 v[106:109], v[66:69], v[170:173], v[106:109]
	ds_write_b32 v130, v135
	v_cndmask_b32_e64 v130, v196, v136, s[2:3]
	v_lshl_or_b32 v130, v130, 2, v198
	ds_write_b32 v130, v176
	v_cndmask_b32_e32 v130, v196, v136, vcc
	v_lshl_or_b32 v130, v130, 2, v198
	ds_write_b32 v130, v177
	ds_read_b128 v[130:133], v197 offset:4608
	ds_read_b128 v[134:137], v197 offset:4672
	ds_read_b128 v[170:173], v197 offset:4736
	ds_read_b128 v[174:177], v197 offset:4800
	s_waitcnt vmcnt(15)
	ds_write_b128 v200, v[138:141]
	s_waitcnt vmcnt(13)
	ds_write_b128 v200, v[142:145] offset:1152
	s_waitcnt vmcnt(11)
	ds_write_b128 v200, v[178:181] offset:2304
	s_waitcnt vmcnt(9)
	ds_write_b128 v200, v[182:185] offset:3456
	s_waitcnt lgkmcnt(7)
	v_cvt_pk_bf16_f32 v138, v130, v131
	v_cvt_pk_bf16_f32 v139, v132, v133
	s_waitcnt lgkmcnt(6)
	v_cvt_pk_bf16_f32 v140, v134, v135
	v_cvt_pk_bf16_f32 v141, v136, v137
	v_lshlrev_b32_e32 v142, 16, v138
	v_and_b32_e32 v143, 0xffff0000, v138
	v_mfma_f32_16x16x32_bf16 v[110:113], v[6:9], v[138:141], v[110:113]
	v_add_f32_e64 v130, v130, -v142
	v_add_f32_e64 v131, v131, -v143
	v_lshlrev_b32_e32 v142, 16, v139
	v_and_b32_e32 v143, 0xffff0000, v139
	v_mfma_f32_16x16x32_bf16 v[106:109], v[50:53], v[138:141], v[106:109]
	v_add_f32_e64 v132, v132, -v142
	v_add_f32_e64 v133, v133, -v143
	v_cvt_pk_bf16_f32 v130, v130, v131
	v_cvt_pk_bf16_f32 v131, v132, v133
	v_lshlrev_b32_e32 v132, 16, v140
	v_and_b32_e32 v133, 0xffff0000, v140
	v_mfma_f32_16x16x32_bf16 v[110:113], v[14:17], v[138:141], v[110:113]
	v_add_f32_e64 v132, v134, -v132
	v_add_f32_e64 v133, v135, -v133
	v_lshlrev_b32_e32 v134, 16, v141
	v_and_b32_e32 v135, 0xffff0000, v141
	v_mfma_f32_16x16x32_bf16 v[106:109], v[54:57], v[138:141], v[106:109]
	v_add_f32_e64 v134, v136, -v134
	v_add_f32_e64 v135, v137, -v135
	v_cvt_pk_bf16_f32 v132, v132, v133
	v_cvt_pk_bf16_f32 v133, v134, v135
	v_mfma_f32_16x16x32_bf16 v[142:145], v[138:141], v[138:141], 0
	s_nop 0
	v_mfma_f32_16x16x32_bf16 v[134:137], v[138:141], v[130:133], 0
	s_waitcnt lgkmcnt(5)
	v_cvt_pk_bf16_f32 v138, v170, v171
	v_lshlrev_b32_e32 v140, 16, v138
	v_and_b32_e32 v141, 0xffff0000, v138
	v_mfma_f32_16x16x32_bf16 v[110:113], v[6:9], v[130:133], v[110:113]
	v_cvt_pk_bf16_f32 v139, v172, v173
	v_mfma_f32_16x16x32_bf16 v[106:109], v[50:53], v[130:133], v[106:109]
	v_add_f32_e64 v130, v170, -v140
	v_add_f32_e64 v131, v171, -v141
	s_waitcnt lgkmcnt(4)
	v_cvt_pk_bf16_f32 v140, v174, v175
	v_cvt_pk_bf16_f32 v141, v176, v177
	v_lshlrev_b32_e32 v132, 16, v139
	v_and_b32_e32 v133, 0xffff0000, v139
	v_pk_add_f32 v[132:133], v[172:173], v[132:133] neg_lo:[0,1] neg_hi:[0,1]
	v_cvt_pk_bf16_f32 v130, v130, v131
	v_cvt_pk_bf16_f32 v131, v132, v133
	v_lshlrev_b32_e32 v132, 16, v140
	v_and_b32_e32 v133, 0xffff0000, v140
	v_lshlrev_b32_e32 v170, 16, v141
	v_and_b32_e32 v171, 0xffff0000, v141
	v_mfma_f32_16x16x32_bf16 v[110:113], v[2:5], v[138:141], v[110:113]
	v_add_f32_e64 v132, v174, -v132
	v_add_f32_e64 v133, v175, -v133
	v_pk_add_f32 v[170:171], v[176:177], v[170:171] neg_lo:[0,1] neg_hi:[0,1]
	v_cvt_pk_bf16_f32 v132, v132, v133
	v_cvt_pk_bf16_f32 v133, v170, v171
	v_mfma_f32_16x16x32_bf16 v[106:109], v[42:45], v[138:141], v[106:109]
	v_mfma_f32_16x16x32_bf16 v[142:145], v[138:141], v[138:141], v[142:145]
	v_mfma_f32_16x16x32_bf16 v[134:137], v[138:141], v[130:133], v[134:137]
	v_mfma_f32_16x16x32_bf16 v[110:113], v[10:13], v[138:141], v[110:113]
	s_nop 6
	v_fma_f32 v144, v136, 2.0, v144
	v_fma_f32 v145, v137, 2.0, v145
	v_mfma_f32_16x16x32_bf16 v[136:139], v[46:49], v[138:141], v[106:109]
	v_or_b32_e32 v140, 0xd0, v199
	v_cndmask_b32_e64 v141, v196, v140, s[6:7]
	v_pk_fma_f32 v[134:135], v[134:135], 2.0, v[142:143] op_sel_hi:[1,0,1]
	v_mfma_f32_16x16x32_bf16 v[106:109], v[2:5], v[130:133], v[110:113]
	s_nop 2
	v_lshl_or_b32 v110, v141, 2, v198
	ds_write_b32 v110, v134
	v_cndmask_b32_e64 v134, v196, v140, s[4:5]
	v_mfma_f32_16x16x32_bf16 v[110:113], v[42:45], v[130:133], v[136:139]
	v_lshl_or_b32 v130, v134, 2, v198
	ds_write_b32 v130, v135
	v_cndmask_b32_e64 v130, v196, v140, s[2:3]
	v_lshl_or_b32 v130, v130, 2, v198
	ds_write_b32 v130, v144
	v_cndmask_b32_e32 v130, v196, v140, vcc
	v_lshl_or_b32 v130, v130, 2, v198
	ds_write_b32 v130, v145
	ds_read_b128 v[130:133], v197
	ds_read_b128 v[134:137], v197 offset:64
	ds_read_b128 v[138:141], v197 offset:128
	ds_read_b128 v[142:145], v197 offset:192
	s_waitcnt vmcnt(14)
	ds_write_b128 v200, v[146:149] offset:4608
	s_waitcnt vmcnt(12)
	ds_write_b128 v200, v[150:153] offset:5760
	s_waitcnt vmcnt(10)
	ds_write_b128 v200, v[186:189] offset:6912
	s_waitcnt vmcnt(8)
	ds_write_b128 v200, v[190:193] offset:8064
	s_waitcnt lgkmcnt(7)
	v_cvt_pk_bf16_f32 v146, v130, v131
	v_cvt_pk_bf16_f32 v147, v132, v133
	s_waitcnt lgkmcnt(6)
	v_cvt_pk_bf16_f32 v148, v134, v135
	v_cvt_pk_bf16_f32 v149, v136, v137
	v_lshlrev_b32_e32 v170, 16, v146
	v_and_b32_e32 v171, 0xffff0000, v146
	v_mfma_f32_16x16x32_bf16 v[150:153], v[22:25], v[146:149], 0
	v_add_f32_e64 v130, v130, -v170
	v_add_f32_e64 v131, v131, -v171
	v_lshlrev_b32_e32 v174, 16, v147
	v_and_b32_e32 v175, 0xffff0000, v147
	v_mfma_f32_16x16x32_bf16 v[170:173], v[34:37], v[146:149], 0
	v_add_f32_e64 v132, v132, -v174
	v_add_f32_e64 v133, v133, -v175
	v_cvt_pk_bf16_f32 v130, v130, v131
	v_cvt_pk_bf16_f32 v131, v132, v133
	v_lshlrev_b32_e32 v132, 16, v148
	v_and_b32_e32 v133, 0xffff0000, v148
	v_mfma_f32_16x16x32_bf16 v[150:153], v[30:33], v[146:149], v[150:153]
	v_add_f32_e64 v132, v134, -v132
	v_add_f32_e64 v133, v135, -v133
	v_lshlrev_b32_e32 v134, 16, v149
	v_and_b32_e32 v135, 0xffff0000, v149
	v_mfma_f32_16x16x32_bf16 v[170:173], v[38:41], v[146:149], v[170:173]
	v_add_f32_e64 v134, v136, -v134
	v_add_f32_e64 v135, v137, -v135
	v_cvt_pk_bf16_f32 v132, v132, v133
	v_cvt_pk_bf16_f32 v133, v134, v135
	v_mfma_f32_16x16x32_bf16 v[174:177], v[146:149], v[146:149], 0
	s_nop 0
	v_mfma_f32_16x16x32_bf16 v[134:137], v[146:149], v[130:133], 0
	v_mfma_f32_16x16x32_bf16 v[146:149], v[22:25], v[130:133], v[150:153]
	s_waitcnt lgkmcnt(5)
	s_nop 1
	v_cvt_pk_bf16_f32 v150, v138, v139
	v_cvt_pk_bf16_f32 v151, v140, v141
	v_lshlrev_b32_e32 v152, 16, v150
	v_and_b32_e32 v153, 0xffff0000, v150
	v_mfma_f32_16x16x32_bf16 v[130:133], v[34:37], v[130:133], v[170:173]
	v_add_f32_e64 v138, v138, -v152
	v_add_f32_e64 v139, v139, -v153
	s_waitcnt lgkmcnt(4)
	v_cvt_pk_bf16_f32 v152, v142, v143
	v_cvt_pk_bf16_f32 v153, v144, v145
	v_lshlrev_b32_e32 v170, 16, v151
	v_and_b32_e32 v171, 0xffff0000, v151
	v_pk_add_f32 v[140:141], v[140:141], v[170:171] neg_lo:[0,1] neg_hi:[0,1]
	v_cvt_pk_bf16_f32 v138, v138, v139
	v_mfma_f32_16x16x32_bf16 v[146:149], v[18:21], v[150:153], v[146:149]
	v_cvt_pk_bf16_f32 v139, v140, v141
	v_lshlrev_b32_e32 v140, 16, v152
	v_and_b32_e32 v141, 0xffff0000, v152
	v_pk_add_f32 v[140:141], v[142:143], v[140:141] neg_lo:[0,1] neg_hi:[0,1]
	v_lshlrev_b32_e32 v142, 16, v153
	v_and_b32_e32 v143, 0xffff0000, v153
	v_mfma_f32_16x16x32_bf16 v[130:133], v[66:69], v[150:153], v[130:133]
	v_add_f32_e64 v142, v144, -v142
	v_add_f32_e64 v143, v145, -v143
	v_cvt_pk_bf16_f32 v140, v140, v141
	v_cvt_pk_bf16_f32 v141, v142, v143
	v_mfma_f32_16x16x32_bf16 v[170:173], v[150:153], v[150:153], v[174:177]
	v_mfma_f32_16x16x32_bf16 v[146:149], v[26:29], v[150:153], v[146:149]
	v_mfma_f32_16x16x32_bf16 v[134:137], v[150:153], v[138:141], v[134:137]
	v_mfma_f32_16x16x32_bf16 v[130:133], v[70:73], v[150:153], v[130:133]
	v_or_b32_e32 v150, 0x60, v199
	v_cndmask_b32_e64 v151, v196, v150, s[6:7]
	s_nop 4
	v_pk_fma_f32 v[142:143], v[136:137], 2.0, v[172:173] op_sel_hi:[1,0,1]
	v_pk_fma_f32 v[144:145], v[134:135], 2.0, v[170:171] op_sel_hi:[1,0,1]
	v_mfma_f32_16x16x32_bf16 v[134:137], v[18:21], v[138:141], v[146:149]
	s_nop 2
	v_lshl_or_b32 v146, v151, 2, v198
	ds_write_b32 v146, v144
	v_cndmask_b32_e64 v144, v196, v150, s[4:5]
	v_mfma_f32_16x16x32_bf16 v[130:133], v[66:69], v[138:141], v[130:133]
	v_lshl_or_b32 v138, v144, 2, v198
	ds_write_b32 v138, v145
	v_cndmask_b32_e64 v138, v196, v150, s[2:3]
	v_lshl_or_b32 v138, v138, 2, v198
	ds_write_b32 v138, v142
	v_cndmask_b32_e32 v138, v196, v150, vcc
	v_lshl_or_b32 v138, v138, 2, v198
	ds_write_b32 v138, v143
	ds_read_b128 v[138:141], v197 offset:4608
	ds_read_b128 v[142:145], v197 offset:4672
	ds_read_b128 v[146:149], v197 offset:4736
	ds_read_b128 v[150:153], v197 offset:4800
	s_waitcnt vmcnt(7)
	ds_write_b128 v200, v[114:117]
	s_waitcnt vmcnt(5)
	ds_write_b128 v200, v[118:121] offset:1152
	s_waitcnt vmcnt(3)
	ds_write_b128 v200, v[154:157] offset:2304
	s_waitcnt vmcnt(1)
	ds_write_b128 v200, v[158:161] offset:3456
	s_waitcnt lgkmcnt(7)
	v_cvt_pk_bf16_f32 v114, v138, v139
	v_cvt_pk_bf16_f32 v115, v140, v141
	s_waitcnt lgkmcnt(6)
	v_cvt_pk_bf16_f32 v116, v142, v143
	v_cvt_pk_bf16_f32 v117, v144, v145
	v_lshlrev_b32_e32 v154, 16, v114
	v_and_b32_e32 v155, 0xffff0000, v114
	v_mfma_f32_16x16x32_bf16 v[118:121], v[6:9], v[114:117], v[134:137]
	v_mfma_f32_16x16x32_bf16 v[130:133], v[50:53], v[114:117], v[130:133]
	s_nop 1
	v_lshlrev_b32_e32 v136, 16, v115
	v_and_b32_e32 v137, 0xffff0000, v115
	v_pk_add_f32 v[134:135], v[138:139], v[154:155] neg_lo:[0,1] neg_hi:[0,1]
	v_pk_add_f32 v[136:137], v[140:141], v[136:137] neg_lo:[0,1] neg_hi:[0,1]
	v_cvt_pk_bf16_f32 v134, v134, v135
	v_cvt_pk_bf16_f32 v135, v136, v137
	v_lshlrev_b32_e32 v136, 16, v116
	v_and_b32_e32 v137, 0xffff0000, v116
	v_mfma_f32_16x16x32_bf16 v[118:121], v[14:17], v[114:117], v[118:121]
	v_add_f32_e64 v136, v142, -v136
	v_add_f32_e64 v137, v143, -v137
	v_lshlrev_b32_e32 v142, 16, v117
	v_and_b32_e32 v143, 0xffff0000, v117
	v_mfma_f32_16x16x32_bf16 v[130:133], v[54:57], v[114:117], v[130:133]
	v_add_f32_e64 v142, v144, -v142
	v_add_f32_e64 v143, v145, -v143
	v_cvt_pk_bf16_f32 v136, v136, v137
	v_cvt_pk_bf16_f32 v137, v142, v143
	s_waitcnt lgkmcnt(5)
	v_cvt_pk_bf16_f32 v142, v146, v147
	v_lshlrev_b32_e32 v144, 16, v142
	v_mfma_f32_16x16x32_bf16 v[118:121], v[6:9], v[134:137], v[118:121]
	v_and_b32_e32 v145, 0xffff0000, v142
	v_cvt_pk_bf16_f32 v143, v148, v149
	v_mfma_f32_16x16x32_bf16 v[130:133], v[50:53], v[134:137], v[130:133]
	v_mfma_f32_16x16x32_bf16 v[138:141], v[114:117], v[114:117], 0
	v_mfma_f32_16x16x32_bf16 v[114:117], v[114:117], v[134:137], 0
	v_add_f32_e64 v134, v146, -v144
	v_add_f32_e64 v135, v147, -v145
	s_waitcnt lgkmcnt(4)
	v_cvt_pk_bf16_f32 v144, v150, v151
	v_cvt_pk_bf16_f32 v145, v152, v153
	v_lshlrev_b32_e32 v136, 16, v143
	v_and_b32_e32 v137, 0xffff0000, v143
	v_mfma_f32_16x16x32_bf16 v[118:121], v[2:5], v[142:145], v[118:121]
	v_add_f32_e64 v136, v148, -v136
	v_add_f32_e64 v137, v149, -v137
	v_cvt_pk_bf16_f32 v134, v134, v135
	v_cvt_pk_bf16_f32 v135, v136, v137
	v_lshlrev_b32_e32 v136, 16, v144
	v_and_b32_e32 v137, 0xffff0000, v144
	v_lshlrev_b32_e32 v146, 16, v145
	v_and_b32_e32 v147, 0xffff0000, v145
	v_mfma_f32_16x16x32_bf16 v[130:133], v[42:45], v[142:145], v[130:133]
	v_add_f32_e64 v136, v150, -v136
	v_add_f32_e64 v137, v151, -v137
	v_pk_add_f32 v[146:147], v[152:153], v[146:147] neg_lo:[0,1] neg_hi:[0,1]
	v_cvt_pk_bf16_f32 v136, v136, v137
	v_cvt_pk_bf16_f32 v137, v146, v147
	v_mfma_f32_16x16x32_bf16 v[138:141], v[142:145], v[142:145], v[138:141]
	v_mfma_f32_16x16x32_bf16 v[118:121], v[10:13], v[142:145], v[118:121]
	v_mfma_f32_16x16x32_bf16 v[114:117], v[142:145], v[134:137], v[114:117]
	v_mfma_f32_16x16x32_bf16 v[130:133], v[46:49], v[142:145], v[130:133]
	v_or_b32_e32 v142, 0xe0, v199
	v_cndmask_b32_e64 v143, v196, v142, s[6:7]
	s_nop 4
	v_pk_fma_f32 v[140:141], v[116:117], 2.0, v[140:141] op_sel_hi:[1,0,1]
	v_pk_fma_f32 v[138:139], v[114:115], 2.0, v[138:139] op_sel_hi:[1,0,1]
	v_mfma_f32_16x16x32_bf16 v[114:117], v[2:5], v[134:137], v[118:121]
	s_nop 2
	v_lshl_or_b32 v118, v143, 2, v198
	ds_write_b32 v118, v138
	v_cndmask_b32_e64 v138, v196, v142, s[4:5]
	v_mfma_f32_16x16x32_bf16 v[118:121], v[42:45], v[134:137], v[130:133]
	s_nop 2
	v_lshl_or_b32 v130, v138, 2, v198
	ds_write_b32 v130, v139
	v_cndmask_b32_e64 v130, v196, v142, s[2:3]
	v_lshl_or_b32 v130, v130, 2, v198
	ds_write_b32 v130, v140
	v_cndmask_b32_e32 v130, v196, v142, vcc
	v_lshl_or_b32 v130, v130, 2, v198
	ds_write_b32 v130, v141
	ds_read_b128 v[130:133], v197
	ds_read_b128 v[134:137], v197 offset:64
	ds_read_b128 v[138:141], v197 offset:128
	ds_read_b128 v[142:145], v197 offset:192
	s_waitcnt vmcnt(6)
	ds_write_b128 v200, v[122:125] offset:4608
	s_waitcnt vmcnt(4)
	ds_write_b128 v200, v[126:129] offset:5760
	s_waitcnt vmcnt(2)
	ds_write_b128 v200, v[162:165] offset:6912
	s_waitcnt vmcnt(0)
	ds_write_b128 v200, v[166:169] offset:8064
	s_waitcnt lgkmcnt(7)
	v_cvt_pk_bf16_f32 v122, v130, v131
	v_cvt_pk_bf16_f32 v123, v132, v133
	s_waitcnt lgkmcnt(6)
	v_cvt_pk_bf16_f32 v124, v134, v135
	v_cvt_pk_bf16_f32 v125, v136, v137
	v_lshlrev_b32_e32 v146, 16, v122
	v_and_b32_e32 v147, 0xffff0000, v122
	v_mfma_f32_16x16x32_bf16 v[126:129], v[22:25], v[122:125], 0
	v_lshlrev_b32_e32 v150, 16, v123
	v_and_b32_e32 v151, 0xffff0000, v123
	v_pk_add_f32 v[130:131], v[130:131], v[146:147] neg_lo:[0,1] neg_hi:[0,1]
	v_pk_add_f32 v[132:133], v[132:133], v[150:151] neg_lo:[0,1] neg_hi:[0,1]
	v_cvt_pk_bf16_f32 v130, v130, v131
	v_mfma_f32_16x16x32_bf16 v[146:149], v[34:37], v[122:125], 0
	v_cvt_pk_bf16_f32 v131, v132, v133
	v_lshlrev_b32_e32 v132, 16, v124
	v_and_b32_e32 v133, 0xffff0000, v124
	v_mfma_f32_16x16x32_bf16 v[30:33], v[30:33], v[122:125], v[126:129]
	s_nop 2
	v_add_f32_e64 v126, v134, -v132
	v_add_f32_e64 v127, v135, -v133
	v_mfma_f32_16x16x32_bf16 v[38:41], v[38:41], v[122:125], v[146:149]
	v_cvt_pk_bf16_f32 v132, v126, v127
	v_lshlrev_b32_e32 v126, 16, v125
	v_and_b32_e32 v127, 0xffff0000, v125
	v_pk_add_f32 v[126:127], v[136:137], v[126:127] neg_lo:[0,1] neg_hi:[0,1]
	v_mfma_f32_16x16x32_bf16 v[150:153], v[122:125], v[122:125], 0
	v_cvt_pk_bf16_f32 v133, v126, v127
	s_nop 1
	v_mfma_f32_16x16x32_bf16 v[22:25], v[22:25], v[130:133], v[30:33]
	s_waitcnt lgkmcnt(5)
	s_nop 1
	v_cvt_pk_bf16_f32 v30, v138, v139
	v_lshlrev_b32_e32 v32, 16, v30
	v_and_b32_e32 v33, 0xffff0000, v30
	v_pk_add_f32 v[32:33], v[138:139], v[32:33] neg_lo:[0,1] neg_hi:[0,1]
	v_mfma_f32_16x16x32_bf16 v[34:37], v[34:37], v[130:133], v[38:41]
	v_cvt_pk_bf16_f32 v31, v140, v141
	s_nop 1
	v_cvt_pk_bf16_f32 v38, v32, v33
	s_waitcnt lgkmcnt(4)
	v_cvt_pk_bf16_f32 v32, v142, v143
	v_cvt_pk_bf16_f32 v33, v144, v145
	v_lshlrev_b32_e32 v40, 16, v31
	v_and_b32_e32 v41, 0xffff0000, v31
	v_mfma_f32_16x16x32_bf16 v[22:25], v[18:21], v[30:33], v[22:25]
	v_add_f32_e64 v40, v140, -v40
	v_add_f32_e64 v41, v141, -v41
	v_cvt_pk_bf16_f32 v39, v40, v41
	v_mfma_f32_16x16x32_bf16 v[122:125], v[122:125], v[130:133], 0
	v_lshlrev_b32_e32 v40, 16, v32
	v_and_b32_e32 v41, 0xffff0000, v32
	v_lshlrev_b32_e32 v130, 16, v33
	v_and_b32_e32 v131, 0xffff0000, v33
	v_pk_add_f32 v[40:41], v[142:143], v[40:41] neg_lo:[0,1] neg_hi:[0,1]
	v_mfma_f32_16x16x32_bf16 v[22:25], v[26:29], v[30:33], v[22:25]
	v_add_f32_e64 v26, v144, -v130
	v_add_f32_e64 v27, v145, -v131
	v_cvt_pk_bf16_f32 v40, v40, v41
	v_cvt_pk_bf16_f32 v41, v26, v27
	v_mfma_f32_16x16x32_bf16 v[34:37], v[66:69], v[30:33], v[34:37]
	v_mfma_f32_16x16x32_bf16 v[126:129], v[30:33], v[30:33], v[150:153]
	v_mfma_f32_16x16x32_bf16 v[26:29], v[30:33], v[38:41], v[122:125]
	v_mfma_f32_16x16x32_bf16 v[18:21], v[18:21], v[38:41], v[22:25]
	s_nop 6
	v_fma_f32 v122, v28, 2.0, v128
	v_fma_f32 v123, v29, 2.0, v129
	v_mfma_f32_16x16x32_bf16 v[28:31], v[70:73], v[30:33], v[34:37]
	v_or_b32_e32 v32, 0x70, v199
	v_cndmask_b32_e64 v33, v196, v32, s[6:7]
	v_pk_fma_f32 v[26:27], v[26:27], 2.0, v[126:127] op_sel_hi:[1,0,1]
	v_lshl_or_b32 v22, v33, 2, v198
	ds_write_b32 v22, v26
	v_cndmask_b32_e64 v26, v196, v32, s[4:5]
	v_lshl_or_b32 v26, v26, 2, v198
	ds_write_b32 v26, v27
	v_cndmask_b32_e64 v26, v196, v32, s[2:3]
	v_lshl_or_b32 v26, v26, 2, v198
	ds_write_b32 v26, v122
	v_cndmask_b32_e32 v26, v196, v32, vcc
	v_lshl_or_b32 v26, v26, 2, v198
	v_mfma_f32_16x16x32_bf16 v[22:25], v[66:69], v[38:41], v[28:31]
	ds_write_b32 v26, v123
	s_nop 1
	ds_read_b128 v[26:29], v197 offset:4608
	ds_read_b128 v[30:33], v197 offset:4672
	ds_read_b128 v[34:37], v197 offset:4736
	ds_read_b128 v[38:41], v197 offset:4800
	s_waitcnt lgkmcnt(3)
	v_cvt_pk_bf16_f32 v66, v26, v27
	v_cvt_pk_bf16_f32 v67, v28, v29
	s_waitcnt lgkmcnt(2)
	v_cvt_pk_bf16_f32 v68, v30, v31
	v_cvt_pk_bf16_f32 v69, v32, v33
	v_lshlrev_b32_e32 v70, 16, v66
	v_and_b32_e32 v71, 0xffff0000, v66
	v_mfma_f32_16x16x32_bf16 v[18:21], v[6:9], v[66:69], v[18:21]
	v_add_f32_e64 v26, v26, -v70
	v_add_f32_e64 v27, v27, -v71
	v_lshlrev_b32_e32 v70, 16, v67
	v_and_b32_e32 v71, 0xffff0000, v67
	v_mfma_f32_16x16x32_bf16 v[22:25], v[50:53], v[66:69], v[22:25]
	v_add_f32_e64 v28, v28, -v70
	v_add_f32_e64 v29, v29, -v71
	v_cvt_pk_bf16_f32 v26, v26, v27
	v_cvt_pk_bf16_f32 v27, v28, v29
	v_lshlrev_b32_e32 v28, 16, v68
	v_and_b32_e32 v29, 0xffff0000, v68
	v_mfma_f32_16x16x32_bf16 v[14:17], v[14:17], v[66:69], v[18:21]
	s_nop 2
	v_add_f32_e64 v18, v30, -v28
	v_add_f32_e64 v19, v31, -v29
	v_lshlrev_b32_e32 v30, 16, v69
	v_and_b32_e32 v31, 0xffff0000, v69
	v_cvt_pk_bf16_f32 v28, v18, v19
	v_mfma_f32_16x16x32_bf16 v[18:21], v[54:57], v[66:69], v[22:25]
	s_nop 2
	v_add_f32_e64 v22, v32, -v30
	v_add_f32_e64 v23, v33, -v31
	v_mfma_f32_16x16x32_bf16 v[70:73], v[66:69], v[66:69], 0
	v_cvt_pk_bf16_f32 v29, v22, v23
	s_nop 1
	v_mfma_f32_16x16x32_bf16 v[6:9], v[6:9], v[26:29], v[14:17]
	s_waitcnt lgkmcnt(1)
	s_nop 1
	v_cvt_pk_bf16_f32 v14, v34, v35
	v_lshlrev_b32_e32 v16, 16, v14
	v_and_b32_e32 v17, 0xffff0000, v14
	v_pk_add_f32 v[16:17], v[34:35], v[16:17] neg_lo:[0,1] neg_hi:[0,1]
	v_mfma_f32_16x16x32_bf16 v[22:25], v[66:69], v[26:29], 0
	v_cvt_pk_bf16_f32 v15, v36, v37
	v_mfma_f32_16x16x32_bf16 v[18:21], v[50:53], v[26:29], v[18:21]
	v_cvt_pk_bf16_f32 v26, v16, v17
	s_waitcnt lgkmcnt(0)
	v_cvt_pk_bf16_f32 v16, v38, v39
	v_cvt_pk_bf16_f32 v17, v40, v41
	v_lshlrev_b32_e32 v28, 16, v15
	v_and_b32_e32 v29, 0xffff0000, v15
	v_mfma_f32_16x16x32_bf16 v[6:9], v[2:5], v[14:17], v[6:9]
	v_add_f32_e64 v28, v36, -v28
	v_add_f32_e64 v29, v37, -v29
	v_lshlrev_b32_e32 v34, 16, v17
	v_cvt_pk_bf16_f32 v27, v28, v29
	v_lshlrev_b32_e32 v28, 16, v16
	v_and_b32_e32 v29, 0xffff0000, v16
	v_and_b32_e32 v35, 0xffff0000, v17
	v_pk_add_f32 v[28:29], v[38:39], v[28:29] neg_lo:[0,1] neg_hi:[0,1]
	v_mfma_f32_16x16x32_bf16 v[6:9], v[10:13], v[14:17], v[6:9]
	v_add_f32_e64 v10, v40, -v34
	v_add_f32_e64 v11, v41, -v35
	v_cvt_pk_bf16_f32 v28, v28, v29
	v_cvt_pk_bf16_f32 v29, v10, v11
	v_mfma_f32_16x16x32_bf16 v[18:21], v[42:45], v[14:17], v[18:21]
	v_mfma_f32_16x16x32_bf16 v[30:33], v[14:17], v[14:17], v[70:73]
	v_mfma_f32_16x16x32_bf16 v[10:13], v[14:17], v[26:29], v[22:25]
	v_mfma_f32_16x16x32_bf16 v[2:5], v[2:5], v[26:29], v[6:9]
	s_nop 6
	v_fma_f32 v22, v12, 2.0, v32
	v_fma_f32 v23, v13, 2.0, v33
	v_mfma_f32_16x16x32_bf16 v[12:15], v[46:49], v[14:17], v[18:21]
	v_or_b32_e32 v16, 0xf0, v199
	v_cndmask_b32_e64 v17, v196, v16, s[6:7]
	v_pk_fma_f32 v[10:11], v[10:11], 2.0, v[30:31] op_sel_hi:[1,0,1]
	v_lshl_or_b32 v6, v17, 2, v198
	ds_write_b32 v6, v10
	v_cndmask_b32_e64 v10, v196, v16, s[4:5]
	v_lshl_or_b32 v10, v10, 2, v198
	v_mfma_f32_16x16x32_bf16 v[6:9], v[42:45], v[26:29], v[12:15]
	ds_write_b32 v10, v11
	v_cndmask_b32_e64 v10, v196, v16, s[2:3]
	v_lshl_or_b32 v10, v10, 2, v198
	ds_write_b32 v10, v22
	v_cndmask_b32_e32 v10, v196, v16, vcc
	v_lshl_or_b32 v10, v10, 2, v198
	ds_write_b32 v10, v23
